# P8/P18 SwiGLU epilogue hand-written (packed f32 mul/add, no zero-init movs, 32-bit store offsets, groups software-interleaved) + gate loads issued in last K-iteration of P9/P19
# speedup vs baseline: 1.0097x; 1.0097x over previous
; __device__ __forceinline__ unsigned pk4_fp8(float a, float b, float c, float d) { unsigned w = 0u; w = __builtin_amdgcn_cvt_pk_fp8_f32(a, b, w, false); w = __builtin_amdgcn_cvt_pk_fp8_f32(c, d, w, true); return w; }
; __device__ __forceinline__ float silu_mul(float g, float u) { const float e = __builtin_amdgcn_exp2f(-g); return (g * u) * __builtin_amdgcn_rcpf(1.0f + e); }
; __device__ __forceinline__ float clamp448(float v) { return __builtin_amdgcn_fmed3f(v, -448.f, 448.f); }
;     __device__ __forceinline__ void operator()(const f32x4 (&acc)[2][2][4][2], const Unit& u, int wr, int wc, int fr, int fq) const {
;         const int row0 = u.pm * BM + wr * 64 + fr, col0 = u.pn * HALF + wc * 32 + 8 * fq;
; #pragma unroll
;         for (int ai = 0; ai < 2; ++ai)
; #pragma unroll
;             for (int m = 0; m < 4; ++m) { unsigned char* rowp = O + (size_t)(row0 + ai * HALF + m * 16) * ldc + col0;
;                 const f32x4 g0 = acc[ai][0][m][0], g1 = acc[ai][0][m][1], u0 = acc[ai][1][m][0], u1 = acc[ai][1][m][1];
;                 f32x2 w_; unsigned lo = pk4_fp8(clamp448(silu_mul(g0[0], u0[0])), clamp448(silu_mul(g0[1], u0[1])), clamp448(silu_mul(g0[2], u0[2])), clamp448(silu_mul(g0[3], u0[3])));
;                 unsigned hi = pk4_fp8(clamp448(silu_mul(g1[0], u1[0])), clamp448(silu_mul(g1[1], u1[1])), clamp448(silu_mul(g1[2], u1[2])), clamp448(silu_mul(g1[3], u1[3])));
;                 typedef unsigned u32x2_ __attribute__((ext_vector_type(2))); (void)w_; *(u32x2_*)rowp = (u32x2_){lo, hi}; }
;     }
.LBB0_844:
	v_lshl_add_u32 v6, s47, 8, v173
	v_lshl_or_b32 v4, s33, 7, v193
	v_readlane_b32 s4, v255, 9
	v_readlane_b32 s5, v255, 10
	v_lshl_add_u32 v186, v6, 11, v4
	v_mov_b32_e32 v184, 1.0
	v_mov_b32_e32 v185, 1.0
	v_exp_f32_e64 v2, -v158
	v_exp_f32_e64 v3, -v159
	v_exp_f32_e64 v4, -v160
	v_exp_f32_e64 v5, -v161
	v_exp_f32_e64 v6, -v150
	v_exp_f32_e64 v7, -v151
	v_exp_f32_e64 v8, -v152
	v_exp_f32_e64 v9, -v153
	v_pk_add_f32 v[2:3], v[2:3], v[184:185]
	v_pk_add_f32 v[4:5], v[4:5], v[184:185]
	v_pk_add_f32 v[6:7], v[6:7], v[184:185]
	v_pk_add_f32 v[8:9], v[8:9], v[184:185]
	v_rcp_f32_e32 v2, v2
	v_rcp_f32_e32 v3, v3
	v_rcp_f32_e32 v4, v4
	v_rcp_f32_e32 v5, v5
	v_rcp_f32_e32 v6, v6
	v_rcp_f32_e32 v7, v7
	v_rcp_f32_e32 v8, v8
	v_rcp_f32_e32 v9, v9
	v_pk_mul_f32 v[10:11], v[158:159], v[154:155]
	v_pk_mul_f32 v[12:13], v[160:161], v[156:157]
	v_pk_mul_f32 v[14:15], v[150:151], v[146:147]
	v_pk_mul_f32 v[16:17], v[152:153], v[148:149]
	v_pk_mul_f32 v[10:11], v[2:3], v[10:11]
	v_exp_f32_e64 v18, -v142
	v_pk_mul_f32 v[12:13], v[4:5], v[12:13]
	v_exp_f32_e64 v19, -v143
	v_pk_mul_f32 v[14:15], v[6:7], v[14:15]
	v_exp_f32_e64 v20, -v144
	v_pk_mul_f32 v[16:17], v[8:9], v[16:17]
	v_exp_f32_e64 v21, -v145
	v_med3_f32 v10, v10, s35, v201
	v_exp_f32_e64 v22, -v134
	v_med3_f32 v11, v11, s35, v201
	v_exp_f32_e64 v23, -v135
	v_med3_f32 v12, v12, s35, v201
	v_exp_f32_e64 v24, -v136
	v_med3_f32 v13, v13, s35, v201
	v_exp_f32_e64 v25, -v137
	v_med3_f32 v14, v14, s35, v201
	v_pk_add_f32 v[18:19], v[18:19], v[184:185]
	v_med3_f32 v15, v15, s35, v201
	v_pk_add_f32 v[20:21], v[20:21], v[184:185]
	v_med3_f32 v16, v16, s35, v201
	v_pk_add_f32 v[22:23], v[22:23], v[184:185]
	v_med3_f32 v17, v17, s35, v201
	v_pk_add_f32 v[24:25], v[24:25], v[184:185]
	v_cvt_pk_fp8_f32 v182, v10, v11
	v_rcp_f32_e32 v18, v18
	v_cvt_pk_fp8_f32 v183, v14, v15
	v_rcp_f32_e32 v19, v19
	v_cvt_pk_fp8_f32 v182, v12, v13 op_sel:[0,0,1]
	v_rcp_f32_e32 v20, v20
	v_cvt_pk_fp8_f32 v183, v16, v17 op_sel:[0,0,1]
	v_rcp_f32_e32 v21, v21
	s_nop 0
	v_rcp_f32_e32 v22, v22
	global_store_dwordx2 v186, v[182:183], s[4:5]
	v_rcp_f32_e32 v23, v23
	v_rcp_f32_e32 v24, v24
	v_rcp_f32_e32 v25, v25
	v_pk_mul_f32 v[26:27], v[142:143], v[138:139]
	v_pk_mul_f32 v[28:29], v[144:145], v[140:141]
	v_pk_mul_f32 v[30:31], v[134:135], v[130:131]
	v_pk_mul_f32 v[32:33], v[136:137], v[132:133]
	v_pk_mul_f32 v[26:27], v[18:19], v[26:27]
	v_exp_f32_e64 v2, -v126
	v_pk_mul_f32 v[28:29], v[20:21], v[28:29]
	v_exp_f32_e64 v3, -v127
	v_pk_mul_f32 v[30:31], v[22:23], v[30:31]
	v_exp_f32_e64 v4, -v128
	v_pk_mul_f32 v[32:33], v[24:25], v[32:33]
	v_exp_f32_e64 v5, -v129
	v_med3_f32 v26, v26, s35, v201
	v_exp_f32_e64 v6, -v118
	v_med3_f32 v27, v27, s35, v201
	v_exp_f32_e64 v7, -v119
	v_med3_f32 v28, v28, s35, v201
	v_exp_f32_e64 v8, -v120
	v_med3_f32 v29, v29, s35, v201
	v_exp_f32_e64 v9, -v121
	v_med3_f32 v30, v30, s35, v201
	v_pk_add_f32 v[2:3], v[2:3], v[184:185]
	v_med3_f32 v31, v31, s35, v201
	v_pk_add_f32 v[4:5], v[4:5], v[184:185]
	v_med3_f32 v32, v32, s35, v201
	v_pk_add_f32 v[6:7], v[6:7], v[184:185]
	v_med3_f32 v33, v33, s35, v201
	v_pk_add_f32 v[8:9], v[8:9], v[184:185]
	v_cvt_pk_fp8_f32 v182, v26, v27
	v_rcp_f32_e32 v2, v2
	v_cvt_pk_fp8_f32 v183, v30, v31
	v_rcp_f32_e32 v3, v3
	v_cvt_pk_fp8_f32 v182, v28, v29 op_sel:[0,0,1]
	v_rcp_f32_e32 v4, v4
	v_cvt_pk_fp8_f32 v183, v32, v33 op_sel:[0,0,1]
	v_rcp_f32_e32 v5, v5
	v_add_u32_e32 v187, 0x8000, v186
	v_rcp_f32_e32 v6, v6
	global_store_dwordx2 v187, v[182:183], s[4:5]
	v_rcp_f32_e32 v7, v7
	v_rcp_f32_e32 v8, v8
	v_rcp_f32_e32 v9, v9
	v_pk_mul_f32 v[10:11], v[126:127], v[122:123]
	v_pk_mul_f32 v[12:13], v[128:129], v[124:125]
	v_pk_mul_f32 v[14:15], v[118:119], v[114:115]
	v_pk_mul_f32 v[16:17], v[120:121], v[116:117]
	v_pk_mul_f32 v[10:11], v[2:3], v[10:11]
	v_exp_f32_e64 v18, -v110
	v_pk_mul_f32 v[12:13], v[4:5], v[12:13]
	v_exp_f32_e64 v19, -v111
	v_pk_mul_f32 v[14:15], v[6:7], v[14:15]
	v_exp_f32_e64 v20, -v112
	v_pk_mul_f32 v[16:17], v[8:9], v[16:17]
	v_exp_f32_e64 v21, -v113
	v_med3_f32 v10, v10, s35, v201
	v_exp_f32_e64 v22, -v98
	v_med3_f32 v11, v11, s35, v201
	v_exp_f32_e64 v23, -v99
	v_med3_f32 v12, v12, s35, v201
	v_exp_f32_e64 v24, -v100
	v_med3_f32 v13, v13, s35, v201
	v_exp_f32_e64 v25, -v101
	v_med3_f32 v14, v14, s35, v201
	v_pk_add_f32 v[18:19], v[18:19], v[184:185]
	v_med3_f32 v15, v15, s35, v201
	v_pk_add_f32 v[20:21], v[20:21], v[184:185]
	v_med3_f32 v16, v16, s35, v201
	v_pk_add_f32 v[22:23], v[22:23], v[184:185]
	v_med3_f32 v17, v17, s35, v201
	v_pk_add_f32 v[24:25], v[24:25], v[184:185]
	v_cvt_pk_fp8_f32 v182, v10, v11
	v_rcp_f32_e32 v18, v18
	v_cvt_pk_fp8_f32 v183, v14, v15
	v_rcp_f32_e32 v19, v19
	v_cvt_pk_fp8_f32 v182, v12, v13 op_sel:[0,0,1]
	v_rcp_f32_e32 v20, v20
	v_cvt_pk_fp8_f32 v183, v16, v17 op_sel:[0,0,1]
	v_rcp_f32_e32 v21, v21
	v_add_u32_e32 v187, 0x10000, v186
	v_rcp_f32_e32 v22, v22
	global_store_dwordx2 v187, v[182:183], s[4:5]
	v_rcp_f32_e32 v23, v23
	v_rcp_f32_e32 v24, v24
	v_rcp_f32_e32 v25, v25
	v_pk_mul_f32 v[26:27], v[110:111], v[106:107]
	v_pk_mul_f32 v[28:29], v[112:113], v[108:109]
	v_pk_mul_f32 v[30:31], v[98:99], v[94:95]
	v_pk_mul_f32 v[32:33], v[100:101], v[96:97]
	v_pk_mul_f32 v[26:27], v[18:19], v[26:27]
	v_exp_f32_e64 v2, -v82
	v_pk_mul_f32 v[28:29], v[20:21], v[28:29]
	v_exp_f32_e64 v3, -v83
	v_pk_mul_f32 v[30:31], v[22:23], v[30:31]
	v_exp_f32_e64 v4, -v84
	v_pk_mul_f32 v[32:33], v[24:25], v[32:33]
	v_exp_f32_e64 v5, -v85
	v_med3_f32 v26, v26, s35, v201
	v_exp_f32_e64 v6, -v70
	v_med3_f32 v27, v27, s35, v201
	v_exp_f32_e64 v7, -v71
	v_med3_f32 v28, v28, s35, v201
	v_exp_f32_e64 v8, -v72
	v_med3_f32 v29, v29, s35, v201
; __device__ __forceinline__ float silu_mul(float g, float u) { const float e = __builtin_amdgcn_exp2f(-g); return (g * u) * __builtin_amdgcn_rcpf(1.0f + e); }
; __device__ __forceinline__ unsigned pk4_fp8(float a, float b, float c, float d) { unsigned w = 0u; w = __builtin_amdgcn_cvt_pk_fp8_f32(a, b, w, false); w = __builtin_amdgcn_cvt_pk_fp8_f32(c, d, w, true); return w; }
; __device__ __forceinline__ float clamp448(float v) { return __builtin_amdgcn_fmed3f(v, -448.f, 448.f); }
;     __device__ __forceinline__ void operator()(const f32x4 (&acc)[2][2][4][2], const Unit& u, int wr, int wc, int fr, int fq) const {
;         const int row0 = u.pm * BM + wr * 64 + fr, col0 = u.pn * HALF + wc * 32 + 8 * fq;
; #pragma unroll
;         for (int ai = 0; ai < 2; ++ai)
; #pragma unroll
;             for (int m = 0; m < 4; ++m) { unsigned char* rowp = O + (size_t)(row0 + ai * HALF + m * 16) * ldc + col0;
;                 const f32x4 g0 = acc[ai][0][m][0], g1 = acc[ai][0][m][1], u0 = acc[ai][1][m][0], u1 = acc[ai][1][m][1];
;                 f32x2 w_; unsigned lo = pk4_fp8(clamp448(silu_mul(g0[0], u0[0])), clamp448(silu_mul(g0[1], u0[1])), clamp448(silu_mul(g0[2], u0[2])), clamp448(silu_mul(g0[3], u0[3])));
;                 unsigned hi = pk4_fp8(clamp448(silu_mul(g1[0], u1[0])), clamp448(silu_mul(g1[1], u1[1])), clamp448(silu_mul(g1[2], u1[2])), clamp448(silu_mul(g1[3], u1[3])));
;                 typedef unsigned u32x2_ __attribute__((ext_vector_type(2))); (void)w_; *(u32x2_*)rowp = (u32x2_){lo, hi}; }
;     }
	v_exp_f32_e64 v9, -v73
	v_med3_f32 v30, v30, s35, v201
	v_pk_add_f32 v[2:3], v[2:3], v[184:185]
	v_med3_f32 v31, v31, s35, v201
	v_pk_add_f32 v[4:5], v[4:5], v[184:185]
	v_med3_f32 v32, v32, s35, v201
	v_pk_add_f32 v[6:7], v[6:7], v[184:185]
	v_med3_f32 v33, v33, s35, v201
	v_pk_add_f32 v[8:9], v[8:9], v[184:185]
	v_cvt_pk_fp8_f32 v182, v26, v27
	v_rcp_f32_e32 v2, v2
	v_cvt_pk_fp8_f32 v183, v30, v31
	v_rcp_f32_e32 v3, v3
	v_cvt_pk_fp8_f32 v182, v28, v29 op_sel:[0,0,1]
	v_rcp_f32_e32 v4, v4
	v_cvt_pk_fp8_f32 v183, v32, v33 op_sel:[0,0,1]
	v_rcp_f32_e32 v5, v5
	v_add_u32_e32 v187, 0x18000, v186
	v_rcp_f32_e32 v6, v6
	global_store_dwordx2 v187, v[182:183], s[4:5]
	v_rcp_f32_e32 v7, v7
	v_rcp_f32_e32 v8, v8
	v_rcp_f32_e32 v9, v9
	v_pk_mul_f32 v[10:11], v[82:83], v[102:103]
	v_pk_mul_f32 v[12:13], v[84:85], v[104:105]
	v_pk_mul_f32 v[14:15], v[70:71], v[90:91]
	v_pk_mul_f32 v[16:17], v[72:73], v[92:93]
	v_pk_mul_f32 v[10:11], v[2:3], v[10:11]
	v_exp_f32_e64 v18, -v78
	v_pk_mul_f32 v[12:13], v[4:5], v[12:13]
	v_exp_f32_e64 v19, -v79
	v_pk_mul_f32 v[14:15], v[6:7], v[14:15]
	v_exp_f32_e64 v20, -v80
	v_pk_mul_f32 v[16:17], v[8:9], v[16:17]
	v_exp_f32_e64 v21, -v81
	v_med3_f32 v10, v10, s35, v201
	v_exp_f32_e64 v22, -v66
	v_med3_f32 v11, v11, s35, v201
	v_exp_f32_e64 v23, -v67
	v_med3_f32 v12, v12, s35, v201
	v_exp_f32_e64 v24, -v68
	v_med3_f32 v13, v13, s35, v201
	v_exp_f32_e64 v25, -v69
	v_med3_f32 v14, v14, s35, v201
	v_pk_add_f32 v[18:19], v[18:19], v[184:185]
	v_med3_f32 v15, v15, s35, v201
	v_pk_add_f32 v[20:21], v[20:21], v[184:185]
	v_med3_f32 v16, v16, s35, v201
	v_pk_add_f32 v[22:23], v[22:23], v[184:185]
	v_med3_f32 v17, v17, s35, v201
	v_pk_add_f32 v[24:25], v[24:25], v[184:185]
	v_cvt_pk_fp8_f32 v182, v10, v11
	v_rcp_f32_e32 v18, v18
	v_cvt_pk_fp8_f32 v183, v14, v15
	v_rcp_f32_e32 v19, v19
	v_cvt_pk_fp8_f32 v182, v12, v13 op_sel:[0,0,1]
	v_rcp_f32_e32 v20, v20
	v_cvt_pk_fp8_f32 v183, v16, v17 op_sel:[0,0,1]
	v_rcp_f32_e32 v21, v21
	v_add_u32_e32 v187, 0x40000, v186
	v_rcp_f32_e32 v22, v22
	global_store_dwordx2 v187, v[182:183], s[4:5]
	v_rcp_f32_e32 v23, v23
	v_rcp_f32_e32 v24, v24
	v_rcp_f32_e32 v25, v25
	v_pk_mul_f32 v[26:27], v[78:79], v[86:87]
	v_pk_mul_f32 v[28:29], v[80:81], v[88:89]
	v_pk_mul_f32 v[30:31], v[66:67], v[74:75]
	v_pk_mul_f32 v[32:33], v[68:69], v[76:77]
	v_pk_mul_f32 v[26:27], v[18:19], v[26:27]
	v_exp_f32_e64 v2, -v58
	v_pk_mul_f32 v[28:29], v[20:21], v[28:29]
	v_exp_f32_e64 v3, -v59
	v_pk_mul_f32 v[30:31], v[22:23], v[30:31]
	v_exp_f32_e64 v4, -v60
	v_pk_mul_f32 v[32:33], v[24:25], v[32:33]
	v_exp_f32_e64 v5, -v61
	v_med3_f32 v26, v26, s35, v201
	v_exp_f32_e64 v6, -v50
	v_med3_f32 v27, v27, s35, v201
	v_exp_f32_e64 v7, -v51
	v_med3_f32 v28, v28, s35, v201
	v_exp_f32_e64 v8, -v52
	v_med3_f32 v29, v29, s35, v201
	v_exp_f32_e64 v9, -v53
	v_med3_f32 v30, v30, s35, v201
	v_pk_add_f32 v[2:3], v[2:3], v[184:185]
	v_med3_f32 v31, v31, s35, v201
	v_pk_add_f32 v[4:5], v[4:5], v[184:185]
	v_med3_f32 v32, v32, s35, v201
	v_pk_add_f32 v[6:7], v[6:7], v[184:185]
	v_med3_f32 v33, v33, s35, v201
	v_pk_add_f32 v[8:9], v[8:9], v[184:185]
	v_cvt_pk_fp8_f32 v182, v26, v27
	v_rcp_f32_e32 v2, v2
	v_cvt_pk_fp8_f32 v183, v30, v31
	v_rcp_f32_e32 v3, v3
	v_cvt_pk_fp8_f32 v182, v28, v29 op_sel:[0,0,1]
	v_rcp_f32_e32 v4, v4
	v_cvt_pk_fp8_f32 v183, v32, v33 op_sel:[0,0,1]
	v_rcp_f32_e32 v5, v5
	v_add_u32_e32 v187, 0x48000, v186
	v_rcp_f32_e32 v6, v6
	global_store_dwordx2 v187, v[182:183], s[4:5]
	v_rcp_f32_e32 v7, v7
	v_rcp_f32_e32 v8, v8
	v_rcp_f32_e32 v9, v9
	v_pk_mul_f32 v[10:11], v[58:59], v[62:63]
	v_pk_mul_f32 v[12:13], v[60:61], v[64:65]
	v_pk_mul_f32 v[14:15], v[50:51], v[54:55]
	v_pk_mul_f32 v[16:17], v[52:53], v[56:57]
	v_pk_mul_f32 v[10:11], v[2:3], v[10:11]
	v_exp_f32_e64 v18, -v42
	v_pk_mul_f32 v[12:13], v[4:5], v[12:13]
	v_exp_f32_e64 v19, -v43
	v_pk_mul_f32 v[14:15], v[6:7], v[14:15]
	v_exp_f32_e64 v20, -v44
	v_pk_mul_f32 v[16:17], v[8:9], v[16:17]
	v_exp_f32_e64 v21, -v45
	v_med3_f32 v10, v10, s35, v201
	v_exp_f32_e64 v22, -v34
	v_med3_f32 v11, v11, s35, v201
	v_exp_f32_e64 v23, -v35
	v_med3_f32 v12, v12, s35, v201
	v_exp_f32_e64 v24, -v36
	v_med3_f32 v13, v13, s35, v201
	v_exp_f32_e64 v25, -v37
	v_med3_f32 v14, v14, s35, v201
	v_pk_add_f32 v[18:19], v[18:19], v[184:185]
	v_med3_f32 v15, v15, s35, v201
	v_pk_add_f32 v[20:21], v[20:21], v[184:185]
	v_med3_f32 v16, v16, s35, v201
	v_pk_add_f32 v[22:23], v[22:23], v[184:185]
	v_med3_f32 v17, v17, s35, v201
	v_pk_add_f32 v[24:25], v[24:25], v[184:185]
	v_cvt_pk_fp8_f32 v182, v10, v11
	v_rcp_f32_e32 v18, v18
	v_cvt_pk_fp8_f32 v183, v14, v15
	v_rcp_f32_e32 v19, v19
	v_cvt_pk_fp8_f32 v182, v12, v13 op_sel:[0,0,1]
	v_rcp_f32_e32 v20, v20
	v_cvt_pk_fp8_f32 v183, v16, v17 op_sel:[0,0,1]
	v_rcp_f32_e32 v21, v21
	v_add_u32_e32 v187, 0x50000, v186
	v_rcp_f32_e32 v22, v22
	global_store_dwordx2 v187, v[182:183], s[4:5]
	v_rcp_f32_e32 v23, v23
	v_rcp_f32_e32 v24, v24
	v_rcp_f32_e32 v25, v25
	v_pk_mul_f32 v[26:27], v[42:43], v[46:47]
	v_pk_mul_f32 v[28:29], v[44:45], v[48:49]
	v_pk_mul_f32 v[30:31], v[34:35], v[38:39]
	v_pk_mul_f32 v[32:33], v[36:37], v[40:41]
	v_pk_mul_f32 v[26:27], v[18:19], v[26:27]
	v_pk_mul_f32 v[28:29], v[20:21], v[28:29]
	v_pk_mul_f32 v[30:31], v[22:23], v[30:31]
	v_pk_mul_f32 v[32:33], v[24:25], v[32:33]
	v_med3_f32 v26, v26, s35, v201
	v_med3_f32 v27, v27, s35, v201
	v_med3_f32 v28, v28, s35, v201
	v_med3_f32 v29, v29, s35, v201
	v_med3_f32 v30, v30, s35, v201
	v_med3_f32 v31, v31, s35, v201
	v_med3_f32 v32, v32, s35, v201
	v_med3_f32 v33, v33, s35, v201
	v_cvt_pk_fp8_f32 v182, v26, v27
	v_cvt_pk_fp8_f32 v183, v30, v31
	v_cvt_pk_fp8_f32 v182, v28, v29 op_sel:[0,0,1]
	v_cvt_pk_fp8_f32 v183, v32, v33 op_sel:[0,0,1]
	v_add_u32_e32 v187, 0x58000, v186
	global_store_dwordx2 v187, v[182:183], s[4:5]
	s_and_b64 vcc, exec, s[2:3]
	s_mov_b64 s[2:3], -1
	s_cbranch_vccnz .LBB0_835
	s_andn2_b64 vcc, exec, s[8:9]
	s_cbranch_vccnz .LBB0_834
	s_barrier
	s_branch .LBB0_834

; #define PG8_STAGE(bufoff, gbase, voff) do { _Pragma("unroll") for (int _i = 0; _i < 2; ++_i) \
;         __builtin_amdgcn_global_load_lds((const unsigned*)((const char*)(gbase) + (voff)[_i]), (PG8_LAS unsigned*)(lds + (bufoff) + ldsw + _i * 8192), 16, 0, 0); } while (0)
; #define PG8_STAGE_A(bufoff, gbase, h, nx) do { if constexpr (Sched::GATHER) { const unsigned vv_[2] = {(nx) ? vAn[h][0] : vA[h][0], (nx) ? vAn[h][1] : vA[h][1]}; PG8_STAGE(bufoff, gbase, vv_); } \
;         else { PG8_STAGE(bufoff, (gbase) + (h) * hstep, voffA); } } while (0)
; #define PG8_LDA(dst, b, h) do { _Pragma("unroll") for (int m = 0; m < 4; ++m) _Pragma("unroll") for (int k = 0; k < 2; ++k) dst[m][k] = *(const PG8_LAS bf16x8*)(lds + PG8_SA(b, h) + aoff + m * 2048 + k * 1024); } while (0)
; #define PG8_LDB(dst, b, h) do { _Pragma("unroll") for (int n = 0; n < 2; ++n) _Pragma("unroll") for (int k = 0; k < 2; ++k) dst[n][k] = *(const PG8_LAS bf16x8*)(lds + PG8_SB(b, h) + boff + n * 2048 + k * 1024); } while (0)
; #define PG8_WAIT_V(n) asm volatile("s_waitcnt vmcnt(" #n ")" ::: "memory")
; #define PG8_WAIT_L(n) asm volatile("s_waitcnt lgkmcnt(" #n ")" ::: "memory")
; #define PG8_BAR __builtin_amdgcn_s_barrier()
; #define PG8_SCHED __builtin_amdgcn_sched_barrier(0)
;     ...
;             PG8_LDB(B0, 0, 0); PG8_LDB(B1, 0, 1); PG8_SCHED; PG8_LDA(At, 0, 0); PG8_STAGE_A(PG8_SA(1, 1), a1, 1, false);
;             PG8_WAIT_V(8); PG8_WAIT_L(0); PG8_BAR; PG8_MMA(0, 0, At, B0); PG8_MMA(0, 1, At, B1); PG8_BAR; PG8_SCHED;
;             PG8_LDA(At, 0, 1); PG8_STAGE(PG8_SB(0, 0), b2, voffB); PG8_STAGE(PG8_SB(0, 1), b2 + hstepB, voffB); PG8_STAGE_A(PG8_SA(0, 0), a2, 0, last);
;             PG8_WAIT_V(8); PG8_WAIT_L(0); PG8_BAR; PG8_MMA(1, 0, At, B0); PG8_MMA(1, 1, At, B1); PG8_BAR; PG8_SCHED;
.LBB0_895:
	ds_read_b128 v[26:29], v188
	ds_read_b128 v[30:33], v188 offset:1024
	ds_read_b128 v[18:21], v188 offset:2048
	ds_read_b128 v[22:25], v188 offset:3072
	ds_read_b128 v[10:13], v189
	ds_read_b128 v[14:17], v189 offset:1024
	ds_read_b128 v[2:5], v189 offset:2048
	ds_read_b128 v[6:9], v189 offset:3072
	s_add_u32 s24, s22, 0xfffc0080
	s_addc_u32 s25, s23, -1
	s_cmp_eq_u32 s47, 12
	s_cselect_b32 s27, s13, s25
	s_cselect_b32 s26, s21, s24
	s_cselect_b32 s25, s15, s46
	s_cselect_b32 s24, s44, s45
	v_lshl_add_u64 v[218:219], s[22:23], 0, v[170:171]
	s_add_i32 m0, s29, 0xc000
	ds_read_b128 v[178:181], v190
	ds_read_b128 v[182:185], v190 offset:1024
	ds_read_b128 v[194:197], v190 offset:2048
	ds_read_b128 v[198:201], v190 offset:3072
	ds_read_b128 v[202:205], v190 offset:4096
	ds_read_b128 v[206:209], v190 offset:5120
	ds_read_b128 v[210:213], v190 offset:6144
	ds_read_b128 v[214:217], v190 offset:7168
	global_load_lds_dwordx4 v[218:219], off
	v_lshl_add_u64 v[218:219], s[22:23], 0, v[172:173]
	s_add_i32 m0, s29, 0xe000
	s_nop 0
	global_load_lds_dwordx4 v[218:219], off
	s_waitcnt vmcnt(8)
	s_waitcnt lgkmcnt(0)
	s_barrier
	s_setprio 1
	s_nop 3
	s_waitcnt lgkmcnt(0)
	v_mfma_scale_f32_16x16x128_f8f6f4 v[158:161], v[26:33], v[178:185], v[158:161], v191, v192 op_sel_hi:[0,0,0]
	v_mfma_scale_f32_16x16x128_f8f6f4 v[154:157], v[18:25], v[178:185], v[154:157], v191, v192 op_sel_hi:[0,0,0]
	v_mfma_scale_f32_16x16x128_f8f6f4 v[142:145], v[26:33], v[194:201], v[142:145], v191, v192 op_sel_hi:[0,0,0]
	v_mfma_scale_f32_16x16x128_f8f6f4 v[138:141], v[18:25], v[194:201], v[138:141], v191, v192 op_sel_hi:[0,0,0]
	v_mfma_scale_f32_16x16x128_f8f6f4 v[126:129], v[26:33], v[202:209], v[126:129], v191, v192 op_sel_hi:[0,0,0]
	v_mfma_scale_f32_16x16x128_f8f6f4 v[122:125], v[18:25], v[202:209], v[122:125], v191, v192 op_sel_hi:[0,0,0]
	v_mfma_scale_f32_16x16x128_f8f6f4 v[110:113], v[26:33], v[210:217], v[110:113], v191, v192 op_sel_hi:[0,0,0]
	v_mfma_scale_f32_16x16x128_f8f6f4 v[106:109], v[18:25], v[210:217], v[106:109], v191, v192 op_sel_hi:[0,0,0]
	s_setprio 0
	s_setprio 1
	s_nop 3
	v_mfma_scale_f32_16x16x128_f8f6f4 v[150:153], v[10:17], v[178:185], v[150:153], v191, v192 op_sel_hi:[0,0,0]
	v_mfma_scale_f32_16x16x128_f8f6f4 v[146:149], v[2:9], v[178:185], v[146:149], v191, v192 op_sel_hi:[0,0,0]
	v_mfma_scale_f32_16x16x128_f8f6f4 v[134:137], v[10:17], v[194:201], v[134:137], v191, v192 op_sel_hi:[0,0,0]
	v_mfma_scale_f32_16x16x128_f8f6f4 v[130:133], v[2:9], v[194:201], v[130:133], v191, v192 op_sel_hi:[0,0,0]
	v_mfma_scale_f32_16x16x128_f8f6f4 v[118:121], v[10:17], v[202:209], v[118:121], v191, v192 op_sel_hi:[0,0,0]
	v_mfma_scale_f32_16x16x128_f8f6f4 v[114:117], v[2:9], v[202:209], v[114:117], v191, v192 op_sel_hi:[0,0,0]
	v_mfma_scale_f32_16x16x128_f8f6f4 v[102:105], v[10:17], v[210:217], v[102:105], v191, v192 op_sel_hi:[0,0,0]
	v_mfma_scale_f32_16x16x128_f8f6f4 v[98:101], v[2:9], v[210:217], v[98:101], v191, v192 op_sel_hi:[0,0,0]
	s_setprio 0
	s_barrier
	s_add_i32 s48, s40, s28
	v_lshl_add_u64 v[178:179], s[24:25], 0, v[166:167]
	s_mov_b32 m0, s48
	ds_read_b128 v[194:197], v190 offset:16384
	ds_read_b128 v[198:201], v190 offset:17408
	ds_read_b128 v[202:205], v190 offset:18432
	ds_read_b128 v[206:209], v190 offset:19456
	ds_read_b128 v[210:213], v190 offset:20480
	ds_read_b128 v[214:217], v190 offset:21504
	ds_read_b128 v[218:221], v190 offset:22528
	ds_read_b128 v[222:225], v190 offset:23552
	global_load_lds_dwordx4 v[178:179], off
	s_add_i32 m0, s48, 0x2000
	s_add_u32 s48, s24, 0x4000
	v_lshl_add_u64 v[180:181], s[24:25], 0, v[162:163]
	s_addc_u32 s49, s25, 0
	s_add_i32 s50, s41, s28
	global_load_lds_dwordx4 v[180:181], off
	v_lshl_add_u64 v[182:183], s[48:49], 0, v[166:167]
	s_mov_b32 m0, s50
	v_lshl_add_u64 v[184:185], s[26:27], 0, v[164:165]
	global_load_lds_dwordx4 v[182:183], off
	v_lshl_add_u64 v[182:183], s[48:49], 0, v[162:163]
	s_add_i32 m0, s50, 0x2000
	s_nop 0
	global_load_lds_dwordx4 v[182:183], off
	v_lshl_add_u64 v[182:183], s[26:27], 0, v[168:169]
	s_mov_b32 m0, s29
	s_nop 0
	global_load_lds_dwordx4 v[182:183], off
	s_mov_b32 m0, s30
	s_nop 0
	global_load_lds_dwordx4 v[184:185], off
	s_waitcnt vmcnt(8)
	s_waitcnt lgkmcnt(0)
	s_barrier
	s_setprio 1
	s_nop 3
	s_waitcnt lgkmcnt(0)
	v_mfma_scale_f32_16x16x128_f8f6f4 v[94:97], v[26:33], v[194:201], v[94:97], v191, v192 op_sel_hi:[0,0,0]
	v_mfma_scale_f32_16x16x128_f8f6f4 v[90:93], v[18:25], v[194:201], v[90:93], v191, v192 op_sel_hi:[0,0,0]
	v_mfma_scale_f32_16x16x128_f8f6f4 v[78:81], v[26:33], v[202:209], v[78:81], v191, v192 op_sel_hi:[0,0,0]
	v_mfma_scale_f32_16x16x128_f8f6f4 v[74:77], v[18:25], v[202:209], v[74:77], v191, v192 op_sel_hi:[0,0,0]
	v_mfma_scale_f32_16x16x128_f8f6f4 v[62:65], v[26:33], v[210:217], v[62:65], v191, v192 op_sel_hi:[0,0,0]
	v_mfma_scale_f32_16x16x128_f8f6f4 v[58:61], v[18:25], v[210:217], v[58:61], v191, v192 op_sel_hi:[0,0,0]
	v_mfma_scale_f32_16x16x128_f8f6f4 v[46:49], v[26:33], v[218:225], v[46:49], v191, v192 op_sel_hi:[0,0,0]
	v_mfma_scale_f32_16x16x128_f8f6f4 v[42:45], v[18:25], v[218:225], v[42:45], v191, v192 op_sel_hi:[0,0,0]
	s_setprio 0
	s_setprio 1
	s_nop 3
	v_mfma_scale_f32_16x16x128_f8f6f4 v[86:89], v[10:17], v[194:201], v[86:89], v191, v192 op_sel_hi:[0,0,0]
	v_mfma_scale_f32_16x16x128_f8f6f4 v[82:85], v[2:9], v[194:201], v[82:85], v191, v192 op_sel_hi:[0,0,0]
	v_mfma_scale_f32_16x16x128_f8f6f4 v[70:73], v[10:17], v[202:209], v[70:73], v191, v192 op_sel_hi:[0,0,0]
	v_mfma_scale_f32_16x16x128_f8f6f4 v[66:69], v[2:9], v[202:209], v[66:69], v191, v192 op_sel_hi:[0,0,0]
	v_mfma_scale_f32_16x16x128_f8f6f4 v[54:57], v[10:17], v[210:217], v[54:57], v191, v192 op_sel_hi:[0,0,0]
	v_mfma_scale_f32_16x16x128_f8f6f4 v[50:53], v[2:9], v[210:217], v[50:53], v191, v192 op_sel_hi:[0,0,0]
	v_mfma_scale_f32_16x16x128_f8f6f4 v[38:41], v[10:17], v[218:225], v[38:41], v191, v192 op_sel_hi:[0,0,0]
	v_mfma_scale_f32_16x16x128_f8f6f4 v[34:37], v[2:9], v[218:225], v[34:37], v191, v192 op_sel_hi:[0,0,0]
	s_setprio 0
	s_barrier
; #define PG8_STAGE(bufoff, gbase, voff) do { _Pragma("unroll") for (int _i = 0; _i < 2; ++_i) \
;         __builtin_amdgcn_global_load_lds((const unsigned*)((const char*)(gbase) + (voff)[_i]), (PG8_LAS unsigned*)(lds + (bufoff) + ldsw + _i * 8192), 16, 0, 0); } while (0)
; #define PG8_STAGE_A(bufoff, gbase, h, nx) do { if constexpr (Sched::GATHER) { const unsigned vv_[2] = {(nx) ? vAn[h][0] : vA[h][0], (nx) ? vAn[h][1] : vA[h][1]}; PG8_STAGE(bufoff, gbase, vv_); } \
;         else { PG8_STAGE(bufoff, (gbase) + (h) * hstep, voffA); } } while (0)
; #define PG8_LDA(dst, b, h) do { _Pragma("unroll") for (int m = 0; m < 4; ++m) _Pragma("unroll") for (int k = 0; k < 2; ++k) dst[m][k] = *(const PG8_LAS bf16x8*)(lds + PG8_SA(b, h) + aoff + m * 2048 + k * 1024); } while (0)
; #define PG8_LDB(dst, b, h) do { _Pragma("unroll") for (int n = 0; n < 2; ++n) _Pragma("unroll") for (int k = 0; k < 2; ++k) dst[n][k] = *(const PG8_LAS bf16x8*)(lds + PG8_SB(b, h) + boff + n * 2048 + k * 1024); } while (0)
; #define PG8_WAIT_V(n) asm volatile("s_waitcnt vmcnt(" #n ")" ::: "memory")
; #define PG8_WAIT_L(n) asm volatile("s_waitcnt lgkmcnt(" #n ")" ::: "memory")
; #define PG8_BAR __builtin_amdgcn_s_barrier()
; #define PG8_SCHED __builtin_amdgcn_sched_barrier(0)
;     ...
;             PG8_LDB(B0, 1, 0); PG8_LDB(B1, 1, 1); PG8_SCHED; PG8_LDA(At, 1, 0); PG8_STAGE_A(PG8_SA(0, 1), a2, 1, last);
;             PG8_WAIT_V(8); PG8_WAIT_L(0); PG8_BAR; PG8_MMA(0, 0, At, B0); PG8_MMA(0, 1, At, B1); PG8_BAR; PG8_SCHED;
;             PG8_LDA(At, 1, 1); PG8_STAGE(PG8_SB(1, 0), b3, voffB); PG8_STAGE(PG8_SB(1, 1), b3 + hstepB, voffB); PG8_STAGE_A(PG8_SA(1, 0), a3, 0, last);
;             PG8_WAIT_V(8); PG8_WAIT_L(0); PG8_BAR; PG8_MMA(1, 0, At, B0); PG8_MMA(1, 1, At, B1); PG8_BAR; PG8_SCHED;
;     __device__ __forceinline__ void operator()(const f32x4 (&acc)[2][2][4][2], const Unit& u, int wr, int wc, int fr, int fq) const {
;     ...
;             for (int m = 0; m < 4; ++m) { const int row = row0 + ai * HALF + m * 16; const float gt = gate[row] * YSCALE; unsigned char* rowp = O + (size_t)row * ldc + col0;
	s_add_i32 s48, 0, 0x18000
	s_add_i32 s49, 0, 0x1c000
	v_add_u32_e32 v14, s48, v186
	v_add_u32_e32 v30, s49, v186
	ds_read_b128 v[2:5], v14
	ds_read_b128 v[6:9], v14 offset:1024
	ds_read_b128 v[10:13], v14 offset:2048
	ds_read_b128 v[14:17], v14 offset:3072
	ds_read_b128 v[18:21], v30
	ds_read_b128 v[22:25], v30 offset:1024
	ds_read_b128 v[26:29], v30 offset:2048
	ds_read_b128 v[30:33], v30 offset:3072
	s_add_u32 s26, s26, 0x40000
	s_addc_u32 s27, s27, 0
	s_mov_b32 m0, s31
	v_lshl_add_u64 v[226:227], s[26:27], 0, v[168:169]
	ds_read_b128 v[194:197], v190 offset:32768
	ds_read_b128 v[198:201], v190 offset:33792
	ds_read_b128 v[202:205], v190 offset:34816
	ds_read_b128 v[206:209], v190 offset:35840
	ds_read_b128 v[210:213], v190 offset:36864
	ds_read_b128 v[214:217], v190 offset:37888
	ds_read_b128 v[218:221], v190 offset:38912
	ds_read_b128 v[222:225], v190 offset:39936
	global_load_lds_dwordx4 v[226:227], off
	v_lshl_add_u64 v[226:227], s[26:27], 0, v[164:165]
	s_mov_b32 m0, s34
	s_nop 0
	global_load_lds_dwordx4 v[226:227], off
	s_waitcnt vmcnt(8)
	s_waitcnt lgkmcnt(0)
	s_barrier
	s_setprio 1
	s_nop 3
	s_waitcnt lgkmcnt(0)
	v_mfma_scale_f32_16x16x128_f8f6f4 v[158:161], v[2:9], v[194:201], v[158:161], v191, v192 op_sel_hi:[0,0,0]
	v_mfma_scale_f32_16x16x128_f8f6f4 v[154:157], v[10:17], v[194:201], v[154:157], v191, v192 op_sel_hi:[0,0,0]
	v_mfma_scale_f32_16x16x128_f8f6f4 v[142:145], v[2:9], v[202:209], v[142:145], v191, v192 op_sel_hi:[0,0,0]
	v_mfma_scale_f32_16x16x128_f8f6f4 v[138:141], v[10:17], v[202:209], v[138:141], v191, v192 op_sel_hi:[0,0,0]
	v_mfma_scale_f32_16x16x128_f8f6f4 v[126:129], v[2:9], v[210:217], v[126:129], v191, v192 op_sel_hi:[0,0,0]
	v_mfma_scale_f32_16x16x128_f8f6f4 v[122:125], v[10:17], v[210:217], v[122:125], v191, v192 op_sel_hi:[0,0,0]
	v_mfma_scale_f32_16x16x128_f8f6f4 v[110:113], v[2:9], v[218:225], v[110:113], v191, v192 op_sel_hi:[0,0,0]
	v_mfma_scale_f32_16x16x128_f8f6f4 v[106:109], v[10:17], v[218:225], v[106:109], v191, v192 op_sel_hi:[0,0,0]
	s_setprio 0
	s_setprio 1
	s_nop 3
	v_mfma_scale_f32_16x16x128_f8f6f4 v[150:153], v[18:25], v[194:201], v[150:153], v191, v192 op_sel_hi:[0,0,0]
	v_mfma_scale_f32_16x16x128_f8f6f4 v[146:149], v[26:33], v[194:201], v[146:149], v191, v192 op_sel_hi:[0,0,0]
	v_mfma_scale_f32_16x16x128_f8f6f4 v[134:137], v[18:25], v[202:209], v[134:137], v191, v192 op_sel_hi:[0,0,0]
	v_mfma_scale_f32_16x16x128_f8f6f4 v[130:133], v[26:33], v[202:209], v[130:133], v191, v192 op_sel_hi:[0,0,0]
	v_mfma_scale_f32_16x16x128_f8f6f4 v[118:121], v[18:25], v[210:217], v[118:121], v191, v192 op_sel_hi:[0,0,0]
	v_mfma_scale_f32_16x16x128_f8f6f4 v[114:117], v[26:33], v[210:217], v[114:117], v191, v192 op_sel_hi:[0,0,0]
	v_mfma_scale_f32_16x16x128_f8f6f4 v[102:105], v[18:25], v[218:225], v[102:105], v191, v192 op_sel_hi:[0,0,0]
	v_mfma_scale_f32_16x16x128_f8f6f4 v[98:101], v[26:33], v[218:225], v[98:101], v191, v192 op_sel_hi:[0,0,0]
	s_setprio 0
	s_barrier
	s_add_i32 s26, s48, s28
	v_lshl_add_u64 v[178:179], v[178:179], 0, s[8:9]
	s_mov_b32 m0, s26
	ds_read_b128 v[194:197], v190 offset:49152
	ds_read_b128 v[198:201], v190 offset:50176
	ds_read_b128 v[202:205], v190 offset:51200
	ds_read_b128 v[206:209], v190 offset:52224
	ds_read_b128 v[210:213], v190 offset:53248
	ds_read_b128 v[214:217], v190 offset:54272
	ds_read_b128 v[218:221], v190 offset:55296
	ds_read_b128 v[222:225], v190 offset:56320
	global_load_lds_dwordx4 v[178:179], off
	s_add_i32 m0, s26, 0x2000
	s_add_u32 s24, s24, 0x4080
	v_lshl_add_u64 v[178:179], v[180:181], 0, s[8:9]
	s_addc_u32 s25, s25, 0
	s_add_i32 s26, s49, s28
	global_load_lds_dwordx4 v[178:179], off
	v_lshl_add_u64 v[178:179], s[24:25], 0, v[166:167]
	s_mov_b32 m0, s26
	s_nop 0
	global_load_lds_dwordx4 v[178:179], off
	v_lshl_add_u64 v[178:179], s[24:25], 0, v[162:163]
	s_add_i32 m0, s26, 0x2000
	s_nop 0
	global_load_lds_dwordx4 v[178:179], off
	v_lshl_add_u64 v[178:179], v[182:183], 0, s[8:9]
	s_mov_b32 m0, s38
	s_nop 0
	global_load_lds_dwordx4 v[178:179], off
	v_lshl_add_u64 v[178:179], v[184:185], 0, s[8:9]
	s_mov_b32 m0, s39
	s_nop 0
	global_load_lds_dwordx4 v[178:179], off
	s_waitcnt vmcnt(8)
	s_cmp_eq_u32 s47, 12
	s_cbranch_scc0 .Lgate9_skip
	v_lshl_add_u32 v236, s20, 8, v1
	v_ashrrev_i32_e32 v237, 31, v236
	v_lshl_add_u64 v[236:237], v[236:237], 2, s[0:1]
	global_load_dword v228, v[236:237], off
	global_load_dword v229, v[236:237], off offset:64
	global_load_dword v230, v[236:237], off offset:128
	global_load_dword v231, v[236:237], off offset:192
	global_load_dword v232, v[236:237], off offset:512
	global_load_dword v233, v[236:237], off offset:576
	global_load_dword v234, v[236:237], off offset:640
	global_load_dword v235, v[236:237], off offset:704
; #define PG8_WAIT_V(n) asm volatile("s_waitcnt vmcnt(" #n ")" ::: "memory")
; #define PG8_WAIT_L(n) asm volatile("s_waitcnt lgkmcnt(" #n ")" ::: "memory")
; #define PG8_BAR __builtin_amdgcn_s_barrier()
; #define PG8_SCHED __builtin_amdgcn_sched_barrier(0)
; __device__ __forceinline__ unsigned pk4_fp8(float a, float b, float c, float d) { unsigned w = 0u; w = __builtin_amdgcn_cvt_pk_fp8_f32(a, b, w, false); w = __builtin_amdgcn_cvt_pk_fp8_f32(c, d, w, true); return w; }
; __device__ __forceinline__ float clamp448(float v) { return __builtin_amdgcn_fmed3f(v, -448.f, 448.f); }
;     ...
;             PG8_WAIT_V(8); PG8_WAIT_L(0); PG8_BAR; PG8_MMA(1, 0, At, B0); PG8_MMA(1, 1, At, B1); PG8_BAR; PG8_SCHED;
;     __device__ __forceinline__ void operator()(const f32x4 (&acc)[2][2][4][2], const Unit& u, int wr, int wc, int fr, int fq) const {
;         const int row0 = u.pm * BM + wr * 64 + fr, col0 = u.pn * BM + wc * 64 + 16 * fq;
; #pragma unroll
;         for (int ai = 0; ai < 2; ++ai)
; #pragma unroll
;             for (int m = 0; m < 4; ++m) { const int row = row0 + ai * HALF + m * 16; const float gt = gate[row] * YSCALE; unsigned char* rowp = O + (size_t)row * ldc + col0;
;                 unsigned w[4];
; #pragma unroll
;                 for (int bj = 0; bj < 2; ++bj)
; #pragma unroll
;                     for (int n = 0; n < 2; ++n) { const f32x4 v = acc[ai][bj][m][n] * gt; w[2 * bj + n] = pk4_fp8(clamp448(v[0]), clamp448(v[1]), clamp448(v[2]), clamp448(v[3])); }
;                 *(u32x4*)rowp = (u32x4){w[0], w[1], w[2], w[3]}; }
.Lgate9_skip:
	s_waitcnt lgkmcnt(0)
	s_barrier
	s_setprio 1
	s_nop 3
	s_waitcnt lgkmcnt(0)
	v_mfma_scale_f32_16x16x128_f8f6f4 v[94:97], v[2:9], v[194:201], v[94:97], v191, v192 op_sel_hi:[0,0,0]
	v_mfma_scale_f32_16x16x128_f8f6f4 v[90:93], v[10:17], v[194:201], v[90:93], v191, v192 op_sel_hi:[0,0,0]
	v_mfma_scale_f32_16x16x128_f8f6f4 v[78:81], v[2:9], v[202:209], v[78:81], v191, v192 op_sel_hi:[0,0,0]
	v_mfma_scale_f32_16x16x128_f8f6f4 v[74:77], v[10:17], v[202:209], v[74:77], v191, v192 op_sel_hi:[0,0,0]
	v_mfma_scale_f32_16x16x128_f8f6f4 v[62:65], v[2:9], v[210:217], v[62:65], v191, v192 op_sel_hi:[0,0,0]
	v_mfma_scale_f32_16x16x128_f8f6f4 v[58:61], v[10:17], v[210:217], v[58:61], v191, v192 op_sel_hi:[0,0,0]
	v_mfma_scale_f32_16x16x128_f8f6f4 v[46:49], v[2:9], v[218:225], v[46:49], v191, v192 op_sel_hi:[0,0,0]
	v_mfma_scale_f32_16x16x128_f8f6f4 v[42:45], v[10:17], v[218:225], v[42:45], v191, v192 op_sel_hi:[0,0,0]
	s_setprio 0
	s_setprio 1
	s_nop 3
	v_mfma_scale_f32_16x16x128_f8f6f4 v[86:89], v[18:25], v[194:201], v[86:89], v191, v192 op_sel_hi:[0,0,0]
	v_mfma_scale_f32_16x16x128_f8f6f4 v[82:85], v[26:33], v[194:201], v[82:85], v191, v192 op_sel_hi:[0,0,0]
	v_mfma_scale_f32_16x16x128_f8f6f4 v[70:73], v[18:25], v[202:209], v[70:73], v191, v192 op_sel_hi:[0,0,0]
	v_mfma_scale_f32_16x16x128_f8f6f4 v[66:69], v[26:33], v[202:209], v[66:69], v191, v192 op_sel_hi:[0,0,0]
	v_mfma_scale_f32_16x16x128_f8f6f4 v[54:57], v[18:25], v[210:217], v[54:57], v191, v192 op_sel_hi:[0,0,0]
	v_mfma_scale_f32_16x16x128_f8f6f4 v[50:53], v[26:33], v[210:217], v[50:53], v191, v192 op_sel_hi:[0,0,0]
	v_mfma_scale_f32_16x16x128_f8f6f4 v[38:41], v[18:25], v[218:225], v[38:41], v191, v192 op_sel_hi:[0,0,0]
	v_mfma_scale_f32_16x16x128_f8f6f4 v[34:37], v[26:33], v[218:225], v[34:37], v191, v192 op_sel_hi:[0,0,0]
	s_setprio 0
	s_barrier
	s_add_i32 s47, s47, 2
	s_add_u32 s22, s22, 0x100
	s_addc_u32 s23, s23, 0
	s_add_u32 s45, s45, 0x100
	s_addc_u32 s46, s46, 0
	s_cmp_gt_u32 s47, 13
	s_cbranch_scc0 .LBB0_895
	s_and_b64 vcc, exec, s[10:11]
	s_cbranch_vccz .LBB0_898
	s_barrier
.LBB0_898:
	v_lshl_add_u32 v2, s20, 8, v1
	v_ashrrev_i32_e32 v3, 31, v2
	v_lshl_add_u64 v[6:7], v[2:3], 2, s[0:1]
	v_lshlrev_b64 v[8:9], 10, v[2:3]
	v_lshl_or_b32 v10, s33, 8, v187
	v_ashrrev_i32_e32 v11, 31, v10
	v_lshl_add_u64 v[8:9], s[94:95], 0, v[8:9]
	v_lshl_add_u64 v[8:9], v[8:9], 0, v[10:11]
	s_mov_b32 s13, 0x20000
	s_mov_b64 s[20:21], -1
	s_waitcnt vmcnt(0)
	v_mul_f32_e32 v4, 0x42000000, v228
	v_pk_mul_f32 v[12:13], v[160:161], v[4:5] op_sel_hi:[1,0]
	v_pk_mul_f32 v[14:15], v[158:159], v[4:5] op_sel_hi:[1,0]
	v_med3_f32 v13, v13, s42, v193
	v_med3_f32 v3, v14, s42, v193
	v_med3_f32 v5, v15, s42, v193
	v_med3_f32 v14, v12, s42, v193
	v_mov_b32_e32 v12, 0
	v_cvt_pk_fp8_f32 v12, v3, v5
	v_pk_mul_f32 v[16:17], v[154:155], v[4:5] op_sel_hi:[1,0]
	v_cvt_pk_fp8_f32 v12, v14, v13 op_sel:[0,0,1]
	v_pk_mul_f32 v[14:15], v[156:157], v[4:5] op_sel_hi:[1,0]
	v_med3_f32 v3, v16, s42, v193
	v_med3_f32 v5, v17, s42, v193
	v_mov_b32_e32 v13, 0
	v_cvt_pk_fp8_f32 v13, v3, v5
	v_med3_f32 v14, v14, s42, v193
	v_med3_f32 v15, v15, s42, v193
	v_pk_mul_f32 v[16:17], v[150:151], v[4:5] op_sel_hi:[1,0]
	v_cvt_pk_fp8_f32 v13, v14, v15 op_sel:[0,0,1]
	v_pk_mul_f32 v[14:15], v[152:153], v[4:5] op_sel_hi:[1,0]
	v_med3_f32 v3, v16, s42, v193
	v_med3_f32 v5, v17, s42, v193
	v_med3_f32 v16, v14, s42, v193
	v_mov_b32_e32 v14, 0
	v_cvt_pk_fp8_f32 v14, v3, v5
	v_med3_f32 v15, v15, s42, v193
	v_cvt_pk_fp8_f32 v14, v16, v15 op_sel:[0,0,1]
	v_pk_mul_f32 v[16:17], v[148:149], v[4:5] op_sel_hi:[1,0]
	v_pk_mul_f32 v[4:5], v[146:147], v[4:5] op_sel_hi:[1,0]
	v_mov_b32_e32 v15, 0
	v_med3_f32 v3, v4, s42, v193
	v_med3_f32 v4, v5, s42, v193
	v_cvt_pk_fp8_f32 v15, v3, v4
	v_med3_f32 v5, v16, s42, v193
	v_med3_f32 v16, v17, s42, v193
	v_or_b32_e32 v4, 16, v2
	v_cvt_pk_fp8_f32 v15, v5, v16 op_sel:[0,0,1]
	v_ashrrev_i32_e32 v5, 31, v4
	global_store_dwordx4 v[8:9], v[12:15], off
	s_nop 1
	v_lshl_add_u64 v[12:13], v[4:5], 2, s[0:1]
	s_nop 1
	v_lshlrev_b64 v[4:5], 10, v[4:5]
	v_lshl_add_u64 v[4:5], s[94:95], 0, v[4:5]
	v_lshl_add_u64 v[4:5], v[4:5], 0, v[10:11]
	v_mul_f32_e32 v16, 0x42000000, v229
	v_pk_mul_f32 v[12:13], v[144:145], v[16:17] op_sel_hi:[1,0]
	v_pk_mul_f32 v[14:15], v[142:143], v[16:17] op_sel_hi:[1,0]
	v_med3_f32 v13, v13, s42, v193
	v_med3_f32 v3, v14, s42, v193
	v_med3_f32 v14, v15, s42, v193
	v_med3_f32 v15, v12, s42, v193
	v_mov_b32_e32 v12, 0
	v_cvt_pk_fp8_f32 v12, v3, v14
	v_pk_mul_f32 v[18:19], v[138:139], v[16:17] op_sel_hi:[1,0]
	v_cvt_pk_fp8_f32 v12, v15, v13 op_sel:[0,0,1]
	v_pk_mul_f32 v[14:15], v[140:141], v[16:17] op_sel_hi:[1,0]
	v_med3_f32 v3, v18, s42, v193
	v_med3_f32 v17, v19, s42, v193
	v_mov_b32_e32 v13, 0
	v_cvt_pk_fp8_f32 v13, v3, v17
	v_med3_f32 v14, v14, s42, v193
	v_med3_f32 v15, v15, s42, v193
	v_pk_mul_f32 v[18:19], v[134:135], v[16:17] op_sel_hi:[1,0]
	v_cvt_pk_fp8_f32 v13, v14, v15 op_sel:[0,0,1]
	v_pk_mul_f32 v[14:15], v[136:137], v[16:17] op_sel_hi:[1,0]
	v_med3_f32 v3, v18, s42, v193
	v_med3_f32 v17, v19, s42, v193
	v_med3_f32 v18, v14, s42, v193
	v_mov_b32_e32 v14, 0
	v_cvt_pk_fp8_f32 v14, v3, v17
	v_med3_f32 v15, v15, s42, v193
	v_cvt_pk_fp8_f32 v14, v18, v15 op_sel:[0,0,1]
	v_pk_mul_f32 v[18:19], v[132:133], v[16:17] op_sel_hi:[1,0]
	v_pk_mul_f32 v[16:17], v[130:131], v[16:17] op_sel_hi:[1,0]
	v_mov_b32_e32 v15, 0
	v_med3_f32 v3, v16, s42, v193
	v_med3_f32 v16, v17, s42, v193
	v_cvt_pk_fp8_f32 v15, v3, v16
	v_med3_f32 v17, v18, s42, v193
	v_med3_f32 v18, v19, s42, v193
	v_cvt_pk_fp8_f32 v15, v17, v18 op_sel:[0,0,1]
	global_store_dwordx4 v[4:5], v[12:15], off
	v_or_b32_e32 v4, 32, v2
; __device__ __forceinline__ unsigned pk4_fp8(float a, float b, float c, float d) { unsigned w = 0u; w = __builtin_amdgcn_cvt_pk_fp8_f32(a, b, w, false); w = __builtin_amdgcn_cvt_pk_fp8_f32(c, d, w, true); return w; }
; __device__ __forceinline__ float clamp448(float v) { return __builtin_amdgcn_fmed3f(v, -448.f, 448.f); }
;     __device__ __forceinline__ void operator()(const f32x4 (&acc)[2][2][4][2], const Unit& u, int wr, int wc, int fr, int fq) const {
;     ...
; #pragma unroll
;         for (int ai = 0; ai < 2; ++ai)
; #pragma unroll
;             for (int m = 0; m < 4; ++m) { const int row = row0 + ai * HALF + m * 16; const float gt = gate[row] * YSCALE; unsigned char* rowp = O + (size_t)row * ldc + col0;
;                 unsigned w[4];
; #pragma unroll
;                 for (int bj = 0; bj < 2; ++bj)
; #pragma unroll
;                     for (int n = 0; n < 2; ++n) { const f32x4 v = acc[ai][bj][m][n] * gt; w[2 * bj + n] = pk4_fp8(clamp448(v[0]), clamp448(v[1]), clamp448(v[2]), clamp448(v[3])); }
;                 *(u32x4*)rowp = (u32x4){w[0], w[1], w[2], w[3]}; }
	v_ashrrev_i32_e32 v5, 31, v4
	v_lshl_add_u64 v[12:13], v[4:5], 2, s[0:1]
	s_nop 1
	v_lshlrev_b64 v[4:5], 10, v[4:5]
	v_lshl_add_u64 v[4:5], s[94:95], 0, v[4:5]
	v_or_b32_e32 v2, 48, v2
	v_lshl_add_u64 v[4:5], v[4:5], 0, v[10:11]
	v_mul_f32_e32 v16, 0x42000000, v230
	v_pk_mul_f32 v[12:13], v[128:129], v[16:17] op_sel_hi:[1,0]
	v_pk_mul_f32 v[14:15], v[126:127], v[16:17] op_sel_hi:[1,0]
	v_med3_f32 v13, v13, s42, v193
	v_med3_f32 v3, v14, s42, v193
	v_med3_f32 v14, v15, s42, v193
	v_med3_f32 v15, v12, s42, v193
	v_mov_b32_e32 v12, 0
	v_cvt_pk_fp8_f32 v12, v3, v14
	v_pk_mul_f32 v[18:19], v[122:123], v[16:17] op_sel_hi:[1,0]
	v_cvt_pk_fp8_f32 v12, v15, v13 op_sel:[0,0,1]
	v_pk_mul_f32 v[14:15], v[124:125], v[16:17] op_sel_hi:[1,0]
	v_med3_f32 v3, v18, s42, v193
	v_med3_f32 v17, v19, s42, v193
	v_mov_b32_e32 v13, 0
	v_cvt_pk_fp8_f32 v13, v3, v17
	v_med3_f32 v14, v14, s42, v193
	v_med3_f32 v15, v15, s42, v193
	v_pk_mul_f32 v[18:19], v[118:119], v[16:17] op_sel_hi:[1,0]
	v_cvt_pk_fp8_f32 v13, v14, v15 op_sel:[0,0,1]
	v_pk_mul_f32 v[14:15], v[120:121], v[16:17] op_sel_hi:[1,0]
	v_med3_f32 v3, v18, s42, v193
	v_med3_f32 v17, v19, s42, v193
	v_med3_f32 v18, v14, s42, v193
	v_mov_b32_e32 v14, 0
	v_cvt_pk_fp8_f32 v14, v3, v17
	v_med3_f32 v15, v15, s42, v193
	v_cvt_pk_fp8_f32 v14, v18, v15 op_sel:[0,0,1]
	v_pk_mul_f32 v[18:19], v[116:117], v[16:17] op_sel_hi:[1,0]
	v_pk_mul_f32 v[16:17], v[114:115], v[16:17] op_sel_hi:[1,0]
	v_mov_b32_e32 v15, 0
	v_med3_f32 v3, v16, s42, v193
	v_med3_f32 v16, v17, s42, v193
	v_cvt_pk_fp8_f32 v15, v3, v16
	v_med3_f32 v17, v18, s42, v193
	v_med3_f32 v18, v19, s42, v193
	v_ashrrev_i32_e32 v3, 31, v2
	v_cvt_pk_fp8_f32 v15, v17, v18 op_sel:[0,0,1]
	global_store_dwordx4 v[4:5], v[12:15], off
	v_lshl_add_u64 v[4:5], v[2:3], 2, s[0:1]
	s_nop 1
	v_lshlrev_b64 v[2:3], 10, v[2:3]
	v_lshl_add_u64 v[12:13], s[94:95], 0, v[2:3]
	v_lshl_add_u64 v[10:11], v[12:13], 0, v[10:11]
	v_mul_f32_e32 v14, 0x42000000, v231
	v_pk_mul_f32 v[2:3], v[112:113], v[14:15] op_sel_hi:[1,0]
	v_pk_mul_f32 v[4:5], v[110:111], v[14:15] op_sel_hi:[1,0]
	v_med3_f32 v15, v2, s42, v193
	v_med3_f32 v4, v4, s42, v193
	v_med3_f32 v5, v5, s42, v193
	v_mov_b32_e32 v2, 0
	v_cvt_pk_fp8_f32 v2, v4, v5
	v_med3_f32 v3, v3, s42, v193
	v_pk_mul_f32 v[16:17], v[106:107], v[14:15] op_sel_hi:[1,0]
	v_pk_mul_f32 v[4:5], v[108:109], v[14:15] op_sel_hi:[1,0]
	v_cvt_pk_fp8_f32 v2, v15, v3 op_sel:[0,0,1]
	v_med3_f32 v15, v16, s42, v193
	v_med3_f32 v16, v17, s42, v193
	v_mov_b32_e32 v3, 0
	v_cvt_pk_fp8_f32 v3, v15, v16
	v_med3_f32 v4, v4, s42, v193
	v_med3_f32 v5, v5, s42, v193
	v_pk_mul_f32 v[16:17], v[102:103], v[14:15] op_sel_hi:[1,0]
	v_cvt_pk_fp8_f32 v3, v4, v5 op_sel:[0,0,1]
	v_pk_mul_f32 v[4:5], v[104:105], v[14:15] op_sel_hi:[1,0]
	v_med3_f32 v15, v16, s42, v193
	v_med3_f32 v16, v17, s42, v193
	v_med3_f32 v17, v4, s42, v193
	v_mov_b32_e32 v4, 0
	v_cvt_pk_fp8_f32 v4, v15, v16
	v_med3_f32 v5, v5, s42, v193
	v_cvt_pk_fp8_f32 v4, v17, v5 op_sel:[0,0,1]
	v_pk_mul_f32 v[16:17], v[100:101], v[14:15] op_sel_hi:[1,0]
	v_pk_mul_f32 v[14:15], v[98:99], v[14:15] op_sel_hi:[1,0]
	v_mov_b32_e32 v5, 0
	v_med3_f32 v14, v14, s42, v193
	v_med3_f32 v15, v15, s42, v193
	v_cvt_pk_fp8_f32 v5, v14, v15
	v_med3_f32 v16, v16, s42, v193
	v_med3_f32 v17, v17, s42, v193
	v_cvt_pk_fp8_f32 v5, v16, v17 op_sel:[0,0,1]
	global_store_dwordx4 v[10:11], v[2:5], off
	s_nop 1
	v_mul_f32_e32 v10, 0x42000000, v232
	v_pk_mul_f32 v[2:3], v[96:97], v[10:11] op_sel_hi:[1,0]
	v_pk_mul_f32 v[4:5], v[94:95], v[10:11] op_sel_hi:[1,0]
	v_med3_f32 v11, v2, s42, v193
	v_med3_f32 v4, v4, s42, v193
	v_med3_f32 v5, v5, s42, v193
	v_mov_b32_e32 v2, 0
	v_cvt_pk_fp8_f32 v2, v4, v5
	v_med3_f32 v3, v3, s42, v193
	v_pk_mul_f32 v[12:13], v[90:91], v[10:11] op_sel_hi:[1,0]
	v_pk_mul_f32 v[4:5], v[92:93], v[10:11] op_sel_hi:[1,0]
	v_cvt_pk_fp8_f32 v2, v11, v3 op_sel:[0,0,1]
	v_med3_f32 v11, v12, s42, v193
	v_med3_f32 v12, v13, s42, v193
	v_mov_b32_e32 v3, 0
	v_cvt_pk_fp8_f32 v3, v11, v12
	v_med3_f32 v4, v4, s42, v193
	v_med3_f32 v5, v5, s42, v193
	v_pk_mul_f32 v[12:13], v[86:87], v[10:11] op_sel_hi:[1,0]
	v_cvt_pk_fp8_f32 v3, v4, v5 op_sel:[0,0,1]
	v_pk_mul_f32 v[4:5], v[88:89], v[10:11] op_sel_hi:[1,0]
	v_med3_f32 v11, v12, s42, v193
	v_med3_f32 v12, v13, s42, v193
	v_med3_f32 v13, v4, s42, v193
	v_mov_b32_e32 v4, 0
	v_cvt_pk_fp8_f32 v4, v11, v12
	v_med3_f32 v5, v5, s42, v193
	v_cvt_pk_fp8_f32 v4, v13, v5 op_sel:[0,0,1]
	v_pk_mul_f32 v[12:13], v[84:85], v[10:11] op_sel_hi:[1,0]
	v_pk_mul_f32 v[10:11], v[82:83], v[10:11] op_sel_hi:[1,0]
	v_mov_b32_e32 v5, 0
	v_med3_f32 v10, v10, s42, v193
	v_med3_f32 v11, v11, s42, v193
	v_cvt_pk_fp8_f32 v5, v10, v11
	v_med3_f32 v12, v12, s42, v193
	v_med3_f32 v13, v13, s42, v193
	v_add_co_u32_e32 v10, vcc, s13, v8
	v_cvt_pk_fp8_f32 v5, v12, v13 op_sel:[0,0,1]
	s_nop 0
; __device__ __forceinline__ unsigned pk4_fp8(float a, float b, float c, float d) { unsigned w = 0u; w = __builtin_amdgcn_cvt_pk_fp8_f32(a, b, w, false); w = __builtin_amdgcn_cvt_pk_fp8_f32(c, d, w, true); return w; }
; __device__ __forceinline__ float clamp448(float v) { return __builtin_amdgcn_fmed3f(v, -448.f, 448.f); }
;     __device__ __forceinline__ void operator()(const f32x4 (&acc)[2][2][4][2], const Unit& u, int wr, int wc, int fr, int fq) const {
;     ...
; #pragma unroll
;         for (int ai = 0; ai < 2; ++ai)
; #pragma unroll
;             for (int m = 0; m < 4; ++m) { const int row = row0 + ai * HALF + m * 16; const float gt = gate[row] * YSCALE; unsigned char* rowp = O + (size_t)row * ldc + col0;
;                 unsigned w[4];
; #pragma unroll
;                 for (int bj = 0; bj < 2; ++bj)
; #pragma unroll
;                     for (int n = 0; n < 2; ++n) { const f32x4 v = acc[ai][bj][m][n] * gt; w[2 * bj + n] = pk4_fp8(clamp448(v[0]), clamp448(v[1]), clamp448(v[2]), clamp448(v[3])); }
;                 *(u32x4*)rowp = (u32x4){w[0], w[1], w[2], w[3]}; }
	v_addc_co_u32_e32 v11, vcc, 0, v9, vcc
	s_mov_b32 s13, 0x24000
	global_store_dwordx4 v[10:11], v[2:5], off
	s_nop 1
	v_mul_f32_e32 v10, 0x42000000, v233
	v_pk_mul_f32 v[2:3], v[80:81], v[10:11] op_sel_hi:[1,0]
	v_pk_mul_f32 v[4:5], v[78:79], v[10:11] op_sel_hi:[1,0]
	v_med3_f32 v11, v2, s42, v193
	v_med3_f32 v4, v4, s42, v193
	v_med3_f32 v5, v5, s42, v193
	v_mov_b32_e32 v2, 0
	v_cvt_pk_fp8_f32 v2, v4, v5
	v_med3_f32 v3, v3, s42, v193
	v_pk_mul_f32 v[12:13], v[74:75], v[10:11] op_sel_hi:[1,0]
	v_pk_mul_f32 v[4:5], v[76:77], v[10:11] op_sel_hi:[1,0]
	v_cvt_pk_fp8_f32 v2, v11, v3 op_sel:[0,0,1]
	v_med3_f32 v11, v12, s42, v193
	v_med3_f32 v12, v13, s42, v193
	v_mov_b32_e32 v3, 0
	v_cvt_pk_fp8_f32 v3, v11, v12
	v_med3_f32 v4, v4, s42, v193
	v_med3_f32 v5, v5, s42, v193
	v_pk_mul_f32 v[12:13], v[70:71], v[10:11] op_sel_hi:[1,0]
	v_cvt_pk_fp8_f32 v3, v4, v5 op_sel:[0,0,1]
	v_pk_mul_f32 v[4:5], v[72:73], v[10:11] op_sel_hi:[1,0]
	v_med3_f32 v11, v12, s42, v193
	v_med3_f32 v12, v13, s42, v193
	v_med3_f32 v13, v4, s42, v193
	v_mov_b32_e32 v4, 0
	v_cvt_pk_fp8_f32 v4, v11, v12
	v_med3_f32 v5, v5, s42, v193
	v_cvt_pk_fp8_f32 v4, v13, v5 op_sel:[0,0,1]
	v_pk_mul_f32 v[12:13], v[68:69], v[10:11] op_sel_hi:[1,0]
	v_pk_mul_f32 v[10:11], v[66:67], v[10:11] op_sel_hi:[1,0]
	v_mov_b32_e32 v5, 0
	v_med3_f32 v10, v10, s42, v193
	v_med3_f32 v11, v11, s42, v193
	v_cvt_pk_fp8_f32 v5, v10, v11
	v_med3_f32 v12, v12, s42, v193
	v_med3_f32 v13, v13, s42, v193
	v_add_co_u32_e32 v10, vcc, s13, v8
	v_cvt_pk_fp8_f32 v5, v12, v13 op_sel:[0,0,1]
	s_nop 0
	v_addc_co_u32_e32 v11, vcc, 0, v9, vcc
	s_mov_b32 s13, 0x28000
	global_store_dwordx4 v[10:11], v[2:5], off
	s_nop 1
	v_mul_f32_e32 v10, 0x42000000, v234
	v_pk_mul_f32 v[2:3], v[64:65], v[10:11] op_sel_hi:[1,0]
	v_pk_mul_f32 v[4:5], v[62:63], v[10:11] op_sel_hi:[1,0]
	v_med3_f32 v11, v2, s42, v193
	v_med3_f32 v4, v4, s42, v193
	v_med3_f32 v5, v5, s42, v193
	v_mov_b32_e32 v2, 0
	v_cvt_pk_fp8_f32 v2, v4, v5
	v_med3_f32 v3, v3, s42, v193
	v_pk_mul_f32 v[12:13], v[58:59], v[10:11] op_sel_hi:[1,0]
	v_pk_mul_f32 v[4:5], v[60:61], v[10:11] op_sel_hi:[1,0]
	v_cvt_pk_fp8_f32 v2, v11, v3 op_sel:[0,0,1]
	v_med3_f32 v11, v12, s42, v193
	v_med3_f32 v12, v13, s42, v193
	v_mov_b32_e32 v3, 0
	v_cvt_pk_fp8_f32 v3, v11, v12
	v_med3_f32 v4, v4, s42, v193
	v_med3_f32 v5, v5, s42, v193
	v_pk_mul_f32 v[12:13], v[54:55], v[10:11] op_sel_hi:[1,0]
	v_cvt_pk_fp8_f32 v3, v4, v5 op_sel:[0,0,1]
	v_pk_mul_f32 v[4:5], v[56:57], v[10:11] op_sel_hi:[1,0]
	v_med3_f32 v11, v12, s42, v193
	v_med3_f32 v12, v13, s42, v193
	v_med3_f32 v13, v4, s42, v193
	v_mov_b32_e32 v4, 0
	v_cvt_pk_fp8_f32 v4, v11, v12
	v_med3_f32 v5, v5, s42, v193
	v_cvt_pk_fp8_f32 v4, v13, v5 op_sel:[0,0,1]
	v_pk_mul_f32 v[12:13], v[52:53], v[10:11] op_sel_hi:[1,0]
	v_pk_mul_f32 v[10:11], v[50:51], v[10:11] op_sel_hi:[1,0]
	v_mov_b32_e32 v5, 0
	v_med3_f32 v10, v10, s42, v193
	v_med3_f32 v11, v11, s42, v193
	v_cvt_pk_fp8_f32 v5, v10, v11
	v_med3_f32 v12, v12, s42, v193
	v_med3_f32 v13, v13, s42, v193
	v_add_co_u32_e32 v10, vcc, s13, v8
	v_cvt_pk_fp8_f32 v5, v12, v13 op_sel:[0,0,1]
	s_nop 0
	v_addc_co_u32_e32 v11, vcc, 0, v9, vcc
	global_store_dwordx4 v[10:11], v[2:5], off
	s_nop 1
	v_mul_f32_e32 v6, 0x42000000, v235
	v_pk_mul_f32 v[2:3], v[48:49], v[6:7] op_sel_hi:[1,0]
	v_pk_mul_f32 v[4:5], v[46:47], v[6:7] op_sel_hi:[1,0]
	v_med3_f32 v7, v2, s42, v193
	v_med3_f32 v4, v4, s42, v193
	v_med3_f32 v5, v5, s42, v193
	v_mov_b32_e32 v2, 0
	v_cvt_pk_fp8_f32 v2, v4, v5
	v_med3_f32 v3, v3, s42, v193
	v_pk_mul_f32 v[10:11], v[42:43], v[6:7] op_sel_hi:[1,0]
	v_pk_mul_f32 v[4:5], v[44:45], v[6:7] op_sel_hi:[1,0]
	v_cvt_pk_fp8_f32 v2, v7, v3 op_sel:[0,0,1]
	v_med3_f32 v7, v10, s42, v193
	v_med3_f32 v10, v11, s42, v193
	v_mov_b32_e32 v3, 0
	v_cvt_pk_fp8_f32 v3, v7, v10
	v_med3_f32 v4, v4, s42, v193
	v_med3_f32 v5, v5, s42, v193
	v_pk_mul_f32 v[10:11], v[38:39], v[6:7] op_sel_hi:[1,0]
	v_cvt_pk_fp8_f32 v3, v4, v5 op_sel:[0,0,1]
	v_pk_mul_f32 v[4:5], v[40:41], v[6:7] op_sel_hi:[1,0]
	v_med3_f32 v7, v10, s42, v193
	v_med3_f32 v10, v11, s42, v193
	v_med3_f32 v11, v4, s42, v193
	v_mov_b32_e32 v4, 0
	v_cvt_pk_fp8_f32 v4, v7, v10
	v_med3_f32 v5, v5, s42, v193
	v_cvt_pk_fp8_f32 v4, v11, v5 op_sel:[0,0,1]
	v_pk_mul_f32 v[10:11], v[36:37], v[6:7] op_sel_hi:[1,0]
	v_pk_mul_f32 v[6:7], v[34:35], v[6:7] op_sel_hi:[1,0]
	v_mov_b32_e32 v5, 0
	v_med3_f32 v6, v6, s42, v193
	v_med3_f32 v7, v7, s42, v193
	v_cvt_pk_fp8_f32 v5, v6, v7
	v_med3_f32 v10, v10, s42, v193
	v_med3_f32 v11, v11, s42, v193
	v_add_co_u32_e32 v6, vcc, 0x2c000, v8
	v_cvt_pk_fp8_f32 v5, v10, v11 op_sel:[0,0,1]
	s_nop 0
	v_addc_co_u32_e32 v7, vcc, 0, v9, vcc
	s_andn2_b64 vcc, exec, s[2:3]
	global_store_dwordx4 v[6:7], v[2:5], off
	s_cbranch_vccnz .LBB0_891
	s_andn2_b64 vcc, exec, s[6:7]
	s_cbranch_vccnz .LBB0_890
	s_barrier
	s_branch .LBB0_890

; __device__ __forceinline__ unsigned pk4_fp8(float a, float b, float c, float d) { unsigned w = 0u; w = __builtin_amdgcn_cvt_pk_fp8_f32(a, b, w, false); w = __builtin_amdgcn_cvt_pk_fp8_f32(c, d, w, true); return w; }
; __device__ __forceinline__ float silu_mul(float g, float u) { const float e = __builtin_amdgcn_exp2f(-g); return (g * u) * __builtin_amdgcn_rcpf(1.0f + e); }
; __device__ __forceinline__ float clamp448(float v) { return __builtin_amdgcn_fmed3f(v, -448.f, 448.f); }
;     __device__ __forceinline__ void operator()(const f32x4 (&acc)[2][2][4][2], const Unit& u, int wr, int wc, int fr, int fq) const {
;         const int row0 = u.pm * BM + wr * 64 + fr, col0 = u.pn * HALF + wc * 32 + 8 * fq;
; #pragma unroll
;         for (int ai = 0; ai < 2; ++ai)
; #pragma unroll
;             for (int m = 0; m < 4; ++m) { unsigned char* rowp = O + (size_t)(row0 + ai * HALF + m * 16) * ldc + col0;
;                 const f32x4 g0 = acc[ai][0][m][0], g1 = acc[ai][0][m][1], u0 = acc[ai][1][m][0], u1 = acc[ai][1][m][1];
;                 f32x2 w_; unsigned lo = pk4_fp8(clamp448(silu_mul(g0[0], u0[0])), clamp448(silu_mul(g0[1], u0[1])), clamp448(silu_mul(g0[2], u0[2])), clamp448(silu_mul(g0[3], u0[3])));
;                 unsigned hi = pk4_fp8(clamp448(silu_mul(g1[0], u1[0])), clamp448(silu_mul(g1[1], u1[1])), clamp448(silu_mul(g1[2], u1[2])), clamp448(silu_mul(g1[3], u1[3])));
;                 typedef unsigned u32x2_ __attribute__((ext_vector_type(2))); (void)w_; *(u32x2_*)rowp = (u32x2_){lo, hi}; }
;     }
.LBB0_1575:
	v_lshl_add_u32 v6, s50, 8, v173
	v_lshl_or_b32 v4, s33, 7, v193
	v_readlane_b32 s4, v255, 9
	v_readlane_b32 s5, v255, 10
	v_lshl_add_u32 v186, v6, 11, v4
	v_mov_b32_e32 v184, 1.0
	v_mov_b32_e32 v185, 1.0
	v_exp_f32_e64 v2, -v158
	v_exp_f32_e64 v3, -v159
	v_exp_f32_e64 v4, -v160
	v_exp_f32_e64 v5, -v161
	v_exp_f32_e64 v6, -v150
	v_exp_f32_e64 v7, -v151
	v_exp_f32_e64 v8, -v152
	v_exp_f32_e64 v9, -v153
	v_pk_add_f32 v[2:3], v[2:3], v[184:185]
	v_pk_add_f32 v[4:5], v[4:5], v[184:185]
	v_pk_add_f32 v[6:7], v[6:7], v[184:185]
	v_pk_add_f32 v[8:9], v[8:9], v[184:185]
	v_rcp_f32_e32 v2, v2
	v_rcp_f32_e32 v3, v3
	v_rcp_f32_e32 v4, v4
	v_rcp_f32_e32 v5, v5
	v_rcp_f32_e32 v6, v6
	v_rcp_f32_e32 v7, v7
	v_rcp_f32_e32 v8, v8
	v_rcp_f32_e32 v9, v9
	v_pk_mul_f32 v[10:11], v[158:159], v[154:155]
	v_pk_mul_f32 v[12:13], v[160:161], v[156:157]
	v_pk_mul_f32 v[14:15], v[150:151], v[146:147]
	v_pk_mul_f32 v[16:17], v[152:153], v[148:149]
	v_pk_mul_f32 v[10:11], v[2:3], v[10:11]
	v_exp_f32_e64 v18, -v142
	v_pk_mul_f32 v[12:13], v[4:5], v[12:13]
	v_exp_f32_e64 v19, -v143
	v_pk_mul_f32 v[14:15], v[6:7], v[14:15]
	v_exp_f32_e64 v20, -v144
	v_pk_mul_f32 v[16:17], v[8:9], v[16:17]
	v_exp_f32_e64 v21, -v145
	v_med3_f32 v10, v10, s35, v201
	v_exp_f32_e64 v22, -v134
	v_med3_f32 v11, v11, s35, v201
	v_exp_f32_e64 v23, -v135
	v_med3_f32 v12, v12, s35, v201
	v_exp_f32_e64 v24, -v136
	v_med3_f32 v13, v13, s35, v201
	v_exp_f32_e64 v25, -v137
	v_med3_f32 v14, v14, s35, v201
	v_pk_add_f32 v[18:19], v[18:19], v[184:185]
	v_med3_f32 v15, v15, s35, v201
	v_pk_add_f32 v[20:21], v[20:21], v[184:185]
	v_med3_f32 v16, v16, s35, v201
	v_pk_add_f32 v[22:23], v[22:23], v[184:185]
	v_med3_f32 v17, v17, s35, v201
	v_pk_add_f32 v[24:25], v[24:25], v[184:185]
	v_cvt_pk_fp8_f32 v182, v10, v11
	v_rcp_f32_e32 v18, v18
	v_cvt_pk_fp8_f32 v183, v14, v15
	v_rcp_f32_e32 v19, v19
	v_cvt_pk_fp8_f32 v182, v12, v13 op_sel:[0,0,1]
	v_rcp_f32_e32 v20, v20
	v_cvt_pk_fp8_f32 v183, v16, v17 op_sel:[0,0,1]
	v_rcp_f32_e32 v21, v21
	s_nop 0
	v_rcp_f32_e32 v22, v22
	global_store_dwordx2 v186, v[182:183], s[4:5]
	v_rcp_f32_e32 v23, v23
	v_rcp_f32_e32 v24, v24
	v_rcp_f32_e32 v25, v25
	v_pk_mul_f32 v[26:27], v[142:143], v[138:139]
	v_pk_mul_f32 v[28:29], v[144:145], v[140:141]
	v_pk_mul_f32 v[30:31], v[134:135], v[130:131]
	v_pk_mul_f32 v[32:33], v[136:137], v[132:133]
	v_pk_mul_f32 v[26:27], v[18:19], v[26:27]
	v_exp_f32_e64 v2, -v126
	v_pk_mul_f32 v[28:29], v[20:21], v[28:29]
	v_exp_f32_e64 v3, -v127
	v_pk_mul_f32 v[30:31], v[22:23], v[30:31]
	v_exp_f32_e64 v4, -v128
	v_pk_mul_f32 v[32:33], v[24:25], v[32:33]
	v_exp_f32_e64 v5, -v129
	v_med3_f32 v26, v26, s35, v201
	v_exp_f32_e64 v6, -v118
	v_med3_f32 v27, v27, s35, v201
	v_exp_f32_e64 v7, -v119
	v_med3_f32 v28, v28, s35, v201
	v_exp_f32_e64 v8, -v120
	v_med3_f32 v29, v29, s35, v201
	v_exp_f32_e64 v9, -v121
	v_med3_f32 v30, v30, s35, v201
	v_pk_add_f32 v[2:3], v[2:3], v[184:185]
	v_med3_f32 v31, v31, s35, v201
	v_pk_add_f32 v[4:5], v[4:5], v[184:185]
	v_med3_f32 v32, v32, s35, v201
	v_pk_add_f32 v[6:7], v[6:7], v[184:185]
	v_med3_f32 v33, v33, s35, v201
	v_pk_add_f32 v[8:9], v[8:9], v[184:185]
	v_cvt_pk_fp8_f32 v182, v26, v27
	v_rcp_f32_e32 v2, v2
	v_cvt_pk_fp8_f32 v183, v30, v31
	v_rcp_f32_e32 v3, v3
	v_cvt_pk_fp8_f32 v182, v28, v29 op_sel:[0,0,1]
	v_rcp_f32_e32 v4, v4
	v_cvt_pk_fp8_f32 v183, v32, v33 op_sel:[0,0,1]
	v_rcp_f32_e32 v5, v5
	v_add_u32_e32 v187, 0x8000, v186
	v_rcp_f32_e32 v6, v6
	global_store_dwordx2 v187, v[182:183], s[4:5]
	v_rcp_f32_e32 v7, v7
	v_rcp_f32_e32 v8, v8
	v_rcp_f32_e32 v9, v9
	v_pk_mul_f32 v[10:11], v[126:127], v[122:123]
	v_pk_mul_f32 v[12:13], v[128:129], v[124:125]
	v_pk_mul_f32 v[14:15], v[118:119], v[114:115]
	v_pk_mul_f32 v[16:17], v[120:121], v[116:117]
	v_pk_mul_f32 v[10:11], v[2:3], v[10:11]
	v_exp_f32_e64 v18, -v110
	v_pk_mul_f32 v[12:13], v[4:5], v[12:13]
	v_exp_f32_e64 v19, -v111
	v_pk_mul_f32 v[14:15], v[6:7], v[14:15]
	v_exp_f32_e64 v20, -v112
	v_pk_mul_f32 v[16:17], v[8:9], v[16:17]
	v_exp_f32_e64 v21, -v113
	v_med3_f32 v10, v10, s35, v201
	v_exp_f32_e64 v22, -v98
	v_med3_f32 v11, v11, s35, v201
	v_exp_f32_e64 v23, -v99
	v_med3_f32 v12, v12, s35, v201
	v_exp_f32_e64 v24, -v100
	v_med3_f32 v13, v13, s35, v201
	v_exp_f32_e64 v25, -v101
	v_med3_f32 v14, v14, s35, v201
	v_pk_add_f32 v[18:19], v[18:19], v[184:185]
	v_med3_f32 v15, v15, s35, v201
	v_pk_add_f32 v[20:21], v[20:21], v[184:185]
	v_med3_f32 v16, v16, s35, v201
	v_pk_add_f32 v[22:23], v[22:23], v[184:185]
	v_med3_f32 v17, v17, s35, v201
	v_pk_add_f32 v[24:25], v[24:25], v[184:185]
	v_cvt_pk_fp8_f32 v182, v10, v11
	v_rcp_f32_e32 v18, v18
	v_cvt_pk_fp8_f32 v183, v14, v15
	v_rcp_f32_e32 v19, v19
	v_cvt_pk_fp8_f32 v182, v12, v13 op_sel:[0,0,1]
	v_rcp_f32_e32 v20, v20
	v_cvt_pk_fp8_f32 v183, v16, v17 op_sel:[0,0,1]
	v_rcp_f32_e32 v21, v21
	v_add_u32_e32 v187, 0x10000, v186
	v_rcp_f32_e32 v22, v22
	global_store_dwordx2 v187, v[182:183], s[4:5]
	v_rcp_f32_e32 v23, v23
	v_rcp_f32_e32 v24, v24
	v_rcp_f32_e32 v25, v25
	v_pk_mul_f32 v[26:27], v[110:111], v[106:107]
	v_pk_mul_f32 v[28:29], v[112:113], v[108:109]
	v_pk_mul_f32 v[30:31], v[98:99], v[94:95]
	v_pk_mul_f32 v[32:33], v[100:101], v[96:97]
	v_pk_mul_f32 v[26:27], v[18:19], v[26:27]
	v_exp_f32_e64 v2, -v82
	v_pk_mul_f32 v[28:29], v[20:21], v[28:29]
	v_exp_f32_e64 v3, -v83
	v_pk_mul_f32 v[30:31], v[22:23], v[30:31]
	v_exp_f32_e64 v4, -v84
	v_pk_mul_f32 v[32:33], v[24:25], v[32:33]
	v_exp_f32_e64 v5, -v85
	v_med3_f32 v26, v26, s35, v201
	v_exp_f32_e64 v6, -v70
	v_med3_f32 v27, v27, s35, v201
	v_exp_f32_e64 v7, -v71
	v_med3_f32 v28, v28, s35, v201
	v_exp_f32_e64 v8, -v72
	v_med3_f32 v29, v29, s35, v201
; __device__ __forceinline__ float silu_mul(float g, float u) { const float e = __builtin_amdgcn_exp2f(-g); return (g * u) * __builtin_amdgcn_rcpf(1.0f + e); }
; __device__ __forceinline__ unsigned pk4_fp8(float a, float b, float c, float d) { unsigned w = 0u; w = __builtin_amdgcn_cvt_pk_fp8_f32(a, b, w, false); w = __builtin_amdgcn_cvt_pk_fp8_f32(c, d, w, true); return w; }
; __device__ __forceinline__ float clamp448(float v) { return __builtin_amdgcn_fmed3f(v, -448.f, 448.f); }
;     __device__ __forceinline__ void operator()(const f32x4 (&acc)[2][2][4][2], const Unit& u, int wr, int wc, int fr, int fq) const {
;         const int row0 = u.pm * BM + wr * 64 + fr, col0 = u.pn * HALF + wc * 32 + 8 * fq;
; #pragma unroll
;         for (int ai = 0; ai < 2; ++ai)
; #pragma unroll
;             for (int m = 0; m < 4; ++m) { unsigned char* rowp = O + (size_t)(row0 + ai * HALF + m * 16) * ldc + col0;
;                 const f32x4 g0 = acc[ai][0][m][0], g1 = acc[ai][0][m][1], u0 = acc[ai][1][m][0], u1 = acc[ai][1][m][1];
;                 f32x2 w_; unsigned lo = pk4_fp8(clamp448(silu_mul(g0[0], u0[0])), clamp448(silu_mul(g0[1], u0[1])), clamp448(silu_mul(g0[2], u0[2])), clamp448(silu_mul(g0[3], u0[3])));
;                 unsigned hi = pk4_fp8(clamp448(silu_mul(g1[0], u1[0])), clamp448(silu_mul(g1[1], u1[1])), clamp448(silu_mul(g1[2], u1[2])), clamp448(silu_mul(g1[3], u1[3])));
;                 typedef unsigned u32x2_ __attribute__((ext_vector_type(2))); (void)w_; *(u32x2_*)rowp = (u32x2_){lo, hi}; }
;     }
	v_exp_f32_e64 v9, -v73
	v_med3_f32 v30, v30, s35, v201
	v_pk_add_f32 v[2:3], v[2:3], v[184:185]
	v_med3_f32 v31, v31, s35, v201
	v_pk_add_f32 v[4:5], v[4:5], v[184:185]
	v_med3_f32 v32, v32, s35, v201
	v_pk_add_f32 v[6:7], v[6:7], v[184:185]
	v_med3_f32 v33, v33, s35, v201
	v_pk_add_f32 v[8:9], v[8:9], v[184:185]
	v_cvt_pk_fp8_f32 v182, v26, v27
	v_rcp_f32_e32 v2, v2
	v_cvt_pk_fp8_f32 v183, v30, v31
	v_rcp_f32_e32 v3, v3
	v_cvt_pk_fp8_f32 v182, v28, v29 op_sel:[0,0,1]
	v_rcp_f32_e32 v4, v4
	v_cvt_pk_fp8_f32 v183, v32, v33 op_sel:[0,0,1]
	v_rcp_f32_e32 v5, v5
	v_add_u32_e32 v187, 0x18000, v186
	v_rcp_f32_e32 v6, v6
	global_store_dwordx2 v187, v[182:183], s[4:5]
	v_rcp_f32_e32 v7, v7
	v_rcp_f32_e32 v8, v8
	v_rcp_f32_e32 v9, v9
	v_pk_mul_f32 v[10:11], v[82:83], v[102:103]
	v_pk_mul_f32 v[12:13], v[84:85], v[104:105]
	v_pk_mul_f32 v[14:15], v[70:71], v[90:91]
	v_pk_mul_f32 v[16:17], v[72:73], v[92:93]
	v_pk_mul_f32 v[10:11], v[2:3], v[10:11]
	v_exp_f32_e64 v18, -v78
	v_pk_mul_f32 v[12:13], v[4:5], v[12:13]
	v_exp_f32_e64 v19, -v79
	v_pk_mul_f32 v[14:15], v[6:7], v[14:15]
	v_exp_f32_e64 v20, -v80
	v_pk_mul_f32 v[16:17], v[8:9], v[16:17]
	v_exp_f32_e64 v21, -v81
	v_med3_f32 v10, v10, s35, v201
	v_exp_f32_e64 v22, -v66
	v_med3_f32 v11, v11, s35, v201
	v_exp_f32_e64 v23, -v67
	v_med3_f32 v12, v12, s35, v201
	v_exp_f32_e64 v24, -v68
	v_med3_f32 v13, v13, s35, v201
	v_exp_f32_e64 v25, -v69
	v_med3_f32 v14, v14, s35, v201
	v_pk_add_f32 v[18:19], v[18:19], v[184:185]
	v_med3_f32 v15, v15, s35, v201
	v_pk_add_f32 v[20:21], v[20:21], v[184:185]
	v_med3_f32 v16, v16, s35, v201
	v_pk_add_f32 v[22:23], v[22:23], v[184:185]
	v_med3_f32 v17, v17, s35, v201
	v_pk_add_f32 v[24:25], v[24:25], v[184:185]
	v_cvt_pk_fp8_f32 v182, v10, v11
	v_rcp_f32_e32 v18, v18
	v_cvt_pk_fp8_f32 v183, v14, v15
	v_rcp_f32_e32 v19, v19
	v_cvt_pk_fp8_f32 v182, v12, v13 op_sel:[0,0,1]
	v_rcp_f32_e32 v20, v20
	v_cvt_pk_fp8_f32 v183, v16, v17 op_sel:[0,0,1]
	v_rcp_f32_e32 v21, v21
	v_add_u32_e32 v187, 0x40000, v186
	v_rcp_f32_e32 v22, v22
	global_store_dwordx2 v187, v[182:183], s[4:5]
	v_rcp_f32_e32 v23, v23
	v_rcp_f32_e32 v24, v24
	v_rcp_f32_e32 v25, v25
	v_pk_mul_f32 v[26:27], v[78:79], v[86:87]
	v_pk_mul_f32 v[28:29], v[80:81], v[88:89]
	v_pk_mul_f32 v[30:31], v[66:67], v[74:75]
	v_pk_mul_f32 v[32:33], v[68:69], v[76:77]
	v_pk_mul_f32 v[26:27], v[18:19], v[26:27]
	v_exp_f32_e64 v2, -v58
	v_pk_mul_f32 v[28:29], v[20:21], v[28:29]
	v_exp_f32_e64 v3, -v59
	v_pk_mul_f32 v[30:31], v[22:23], v[30:31]
	v_exp_f32_e64 v4, -v60
	v_pk_mul_f32 v[32:33], v[24:25], v[32:33]
	v_exp_f32_e64 v5, -v61
	v_med3_f32 v26, v26, s35, v201
	v_exp_f32_e64 v6, -v50
	v_med3_f32 v27, v27, s35, v201
	v_exp_f32_e64 v7, -v51
	v_med3_f32 v28, v28, s35, v201
	v_exp_f32_e64 v8, -v52
	v_med3_f32 v29, v29, s35, v201
	v_exp_f32_e64 v9, -v53
	v_med3_f32 v30, v30, s35, v201
	v_pk_add_f32 v[2:3], v[2:3], v[184:185]
	v_med3_f32 v31, v31, s35, v201
	v_pk_add_f32 v[4:5], v[4:5], v[184:185]
	v_med3_f32 v32, v32, s35, v201
	v_pk_add_f32 v[6:7], v[6:7], v[184:185]
	v_med3_f32 v33, v33, s35, v201
	v_pk_add_f32 v[8:9], v[8:9], v[184:185]
	v_cvt_pk_fp8_f32 v182, v26, v27
	v_rcp_f32_e32 v2, v2
	v_cvt_pk_fp8_f32 v183, v30, v31
	v_rcp_f32_e32 v3, v3
	v_cvt_pk_fp8_f32 v182, v28, v29 op_sel:[0,0,1]
	v_rcp_f32_e32 v4, v4
	v_cvt_pk_fp8_f32 v183, v32, v33 op_sel:[0,0,1]
	v_rcp_f32_e32 v5, v5
	v_add_u32_e32 v187, 0x48000, v186
	v_rcp_f32_e32 v6, v6
	global_store_dwordx2 v187, v[182:183], s[4:5]
	v_rcp_f32_e32 v7, v7
	v_rcp_f32_e32 v8, v8
	v_rcp_f32_e32 v9, v9
	v_pk_mul_f32 v[10:11], v[58:59], v[62:63]
	v_pk_mul_f32 v[12:13], v[60:61], v[64:65]
	v_pk_mul_f32 v[14:15], v[50:51], v[54:55]
	v_pk_mul_f32 v[16:17], v[52:53], v[56:57]
	v_pk_mul_f32 v[10:11], v[2:3], v[10:11]
	v_exp_f32_e64 v18, -v42
	v_pk_mul_f32 v[12:13], v[4:5], v[12:13]
	v_exp_f32_e64 v19, -v43
	v_pk_mul_f32 v[14:15], v[6:7], v[14:15]
	v_exp_f32_e64 v20, -v44
	v_pk_mul_f32 v[16:17], v[8:9], v[16:17]
	v_exp_f32_e64 v21, -v45
	v_med3_f32 v10, v10, s35, v201
	v_exp_f32_e64 v22, -v34
	v_med3_f32 v11, v11, s35, v201
	v_exp_f32_e64 v23, -v35
	v_med3_f32 v12, v12, s35, v201
	v_exp_f32_e64 v24, -v36
	v_med3_f32 v13, v13, s35, v201
	v_exp_f32_e64 v25, -v37
	v_med3_f32 v14, v14, s35, v201
	v_pk_add_f32 v[18:19], v[18:19], v[184:185]
	v_med3_f32 v15, v15, s35, v201
	v_pk_add_f32 v[20:21], v[20:21], v[184:185]
	v_med3_f32 v16, v16, s35, v201
	v_pk_add_f32 v[22:23], v[22:23], v[184:185]
	v_med3_f32 v17, v17, s35, v201
	v_pk_add_f32 v[24:25], v[24:25], v[184:185]
	v_cvt_pk_fp8_f32 v182, v10, v11
	v_rcp_f32_e32 v18, v18
	v_cvt_pk_fp8_f32 v183, v14, v15
	v_rcp_f32_e32 v19, v19
	v_cvt_pk_fp8_f32 v182, v12, v13 op_sel:[0,0,1]
	v_rcp_f32_e32 v20, v20
	v_cvt_pk_fp8_f32 v183, v16, v17 op_sel:[0,0,1]
	v_rcp_f32_e32 v21, v21
	v_add_u32_e32 v187, 0x50000, v186
	v_rcp_f32_e32 v22, v22
	global_store_dwordx2 v187, v[182:183], s[4:5]
	v_rcp_f32_e32 v23, v23
	v_rcp_f32_e32 v24, v24
	v_rcp_f32_e32 v25, v25
	v_pk_mul_f32 v[26:27], v[42:43], v[46:47]
	v_pk_mul_f32 v[28:29], v[44:45], v[48:49]
	v_pk_mul_f32 v[30:31], v[34:35], v[38:39]
	v_pk_mul_f32 v[32:33], v[36:37], v[40:41]
	v_pk_mul_f32 v[26:27], v[18:19], v[26:27]
	v_pk_mul_f32 v[28:29], v[20:21], v[28:29]
	v_pk_mul_f32 v[30:31], v[22:23], v[30:31]
	v_pk_mul_f32 v[32:33], v[24:25], v[32:33]
	v_med3_f32 v26, v26, s35, v201
	v_med3_f32 v27, v27, s35, v201
	v_med3_f32 v28, v28, s35, v201
	v_med3_f32 v29, v29, s35, v201
	v_med3_f32 v30, v30, s35, v201
	v_med3_f32 v31, v31, s35, v201
	v_med3_f32 v32, v32, s35, v201
	v_med3_f32 v33, v33, s35, v201
	v_cvt_pk_fp8_f32 v182, v26, v27
	v_cvt_pk_fp8_f32 v183, v30, v31
	v_cvt_pk_fp8_f32 v182, v28, v29 op_sel:[0,0,1]
	v_cvt_pk_fp8_f32 v183, v32, v33 op_sel:[0,0,1]
	v_add_u32_e32 v187, 0x58000, v186
	global_store_dwordx2 v187, v[182:183], s[4:5]
	s_and_b64 vcc, exec, s[2:3]
	s_mov_b64 s[2:3], -1
	s_cbranch_vccnz .LBB0_1566
	s_andn2_b64 vcc, exec, s[8:9]
	s_cbranch_vccnz .LBB0_1565
	s_barrier
	s_branch .LBB0_1565

; #define PG8_STAGE(bufoff, gbase, voff) do { _Pragma("unroll") for (int _i = 0; _i < 2; ++_i) \
;         __builtin_amdgcn_global_load_lds((const unsigned*)((const char*)(gbase) + (voff)[_i]), (PG8_LAS unsigned*)(lds + (bufoff) + ldsw + _i * 8192), 16, 0, 0); } while (0)
; #define PG8_STAGE_A(bufoff, gbase, h, nx) do { if constexpr (Sched::GATHER) { const unsigned vv_[2] = {(nx) ? vAn[h][0] : vA[h][0], (nx) ? vAn[h][1] : vA[h][1]}; PG8_STAGE(bufoff, gbase, vv_); } \
;         else { PG8_STAGE(bufoff, (gbase) + (h) * hstep, voffA); } } while (0)
; #define PG8_LDA(dst, b, h) do { _Pragma("unroll") for (int m = 0; m < 4; ++m) _Pragma("unroll") for (int k = 0; k < 2; ++k) dst[m][k] = *(const PG8_LAS bf16x8*)(lds + PG8_SA(b, h) + aoff + m * 2048 + k * 1024); } while (0)
; #define PG8_LDB(dst, b, h) do { _Pragma("unroll") for (int n = 0; n < 2; ++n) _Pragma("unroll") for (int k = 0; k < 2; ++k) dst[n][k] = *(const PG8_LAS bf16x8*)(lds + PG8_SB(b, h) + boff + n * 2048 + k * 1024); } while (0)
; #define PG8_WAIT_V(n) asm volatile("s_waitcnt vmcnt(" #n ")" ::: "memory")
; #define PG8_WAIT_L(n) asm volatile("s_waitcnt lgkmcnt(" #n ")" ::: "memory")
; #define PG8_BAR __builtin_amdgcn_s_barrier()
; #define PG8_SCHED __builtin_amdgcn_sched_barrier(0)
;     ...
;             PG8_LDB(B0, 0, 0); PG8_LDB(B1, 0, 1); PG8_SCHED; PG8_LDA(At, 0, 0); PG8_STAGE_A(PG8_SA(1, 1), a1, 1, false);
;             PG8_WAIT_V(8); PG8_WAIT_L(0); PG8_BAR; PG8_MMA(0, 0, At, B0); PG8_MMA(0, 1, At, B1); PG8_BAR; PG8_SCHED;
;             PG8_LDA(At, 0, 1); PG8_STAGE(PG8_SB(0, 0), b2, voffB); PG8_STAGE(PG8_SB(0, 1), b2 + hstepB, voffB); PG8_STAGE_A(PG8_SA(0, 0), a2, 0, last);
;             PG8_WAIT_V(8); PG8_WAIT_L(0); PG8_BAR; PG8_MMA(1, 0, At, B0); PG8_MMA(1, 1, At, B1); PG8_BAR; PG8_SCHED;
.LBB0_1626:
	ds_read_b128 v[26:29], v188
	ds_read_b128 v[30:33], v188 offset:1024
	ds_read_b128 v[18:21], v188 offset:2048
	ds_read_b128 v[22:25], v188 offset:3072
	ds_read_b128 v[10:13], v189
	ds_read_b128 v[14:17], v189 offset:1024
	ds_read_b128 v[2:5], v189 offset:2048
	ds_read_b128 v[6:9], v189 offset:3072
	s_add_u32 s24, s22, 0xfffc0080
	s_addc_u32 s25, s23, -1
	s_cmp_eq_u32 s50, 12
	s_cselect_b32 s27, s13, s25
	s_cselect_b32 s26, s46, s24
	s_cselect_b32 s25, s15, s49
	s_cselect_b32 s24, s47, s48
	v_lshl_add_u64 v[218:219], s[22:23], 0, v[170:171]
	s_add_i32 m0, s28, 0xc000
	ds_read_b128 v[178:181], v190
	ds_read_b128 v[182:185], v190 offset:1024
	ds_read_b128 v[194:197], v190 offset:2048
	ds_read_b128 v[198:201], v190 offset:3072
	ds_read_b128 v[202:205], v190 offset:4096
	ds_read_b128 v[206:209], v190 offset:5120
	ds_read_b128 v[210:213], v190 offset:6144
	ds_read_b128 v[214:217], v190 offset:7168
	global_load_lds_dwordx4 v[218:219], off
	v_lshl_add_u64 v[218:219], s[22:23], 0, v[172:173]
	s_add_i32 m0, s28, 0xe000
	s_nop 0
	global_load_lds_dwordx4 v[218:219], off
	s_waitcnt vmcnt(8)
	s_waitcnt lgkmcnt(0)
	s_barrier
	s_setprio 1
	s_nop 3
	s_waitcnt lgkmcnt(0)
	v_mfma_scale_f32_16x16x128_f8f6f4 v[158:161], v[26:33], v[178:185], v[158:161], v191, v192 op_sel_hi:[0,0,0]
	v_mfma_scale_f32_16x16x128_f8f6f4 v[154:157], v[18:25], v[178:185], v[154:157], v191, v192 op_sel_hi:[0,0,0]
	v_mfma_scale_f32_16x16x128_f8f6f4 v[142:145], v[26:33], v[194:201], v[142:145], v191, v192 op_sel_hi:[0,0,0]
	v_mfma_scale_f32_16x16x128_f8f6f4 v[138:141], v[18:25], v[194:201], v[138:141], v191, v192 op_sel_hi:[0,0,0]
	v_mfma_scale_f32_16x16x128_f8f6f4 v[126:129], v[26:33], v[202:209], v[126:129], v191, v192 op_sel_hi:[0,0,0]
	v_mfma_scale_f32_16x16x128_f8f6f4 v[122:125], v[18:25], v[202:209], v[122:125], v191, v192 op_sel_hi:[0,0,0]
	v_mfma_scale_f32_16x16x128_f8f6f4 v[110:113], v[26:33], v[210:217], v[110:113], v191, v192 op_sel_hi:[0,0,0]
	v_mfma_scale_f32_16x16x128_f8f6f4 v[106:109], v[18:25], v[210:217], v[106:109], v191, v192 op_sel_hi:[0,0,0]
	s_setprio 0
	s_setprio 1
	s_nop 3
	v_mfma_scale_f32_16x16x128_f8f6f4 v[150:153], v[10:17], v[178:185], v[150:153], v191, v192 op_sel_hi:[0,0,0]
	v_mfma_scale_f32_16x16x128_f8f6f4 v[146:149], v[2:9], v[178:185], v[146:149], v191, v192 op_sel_hi:[0,0,0]
	v_mfma_scale_f32_16x16x128_f8f6f4 v[134:137], v[10:17], v[194:201], v[134:137], v191, v192 op_sel_hi:[0,0,0]
	v_mfma_scale_f32_16x16x128_f8f6f4 v[130:133], v[2:9], v[194:201], v[130:133], v191, v192 op_sel_hi:[0,0,0]
	v_mfma_scale_f32_16x16x128_f8f6f4 v[118:121], v[10:17], v[202:209], v[118:121], v191, v192 op_sel_hi:[0,0,0]
	v_mfma_scale_f32_16x16x128_f8f6f4 v[114:117], v[2:9], v[202:209], v[114:117], v191, v192 op_sel_hi:[0,0,0]
	v_mfma_scale_f32_16x16x128_f8f6f4 v[102:105], v[10:17], v[210:217], v[102:105], v191, v192 op_sel_hi:[0,0,0]
	v_mfma_scale_f32_16x16x128_f8f6f4 v[98:101], v[2:9], v[210:217], v[98:101], v191, v192 op_sel_hi:[0,0,0]
	s_setprio 0
	s_barrier
	s_add_i32 s51, s39, s21
	v_lshl_add_u64 v[178:179], s[24:25], 0, v[166:167]
	s_mov_b32 m0, s51
	ds_read_b128 v[194:197], v190 offset:16384
	ds_read_b128 v[198:201], v190 offset:17408
	ds_read_b128 v[202:205], v190 offset:18432
	ds_read_b128 v[206:209], v190 offset:19456
	ds_read_b128 v[210:213], v190 offset:20480
	ds_read_b128 v[214:217], v190 offset:21504
	ds_read_b128 v[218:221], v190 offset:22528
	ds_read_b128 v[222:225], v190 offset:23552
	global_load_lds_dwordx4 v[178:179], off
	s_add_i32 m0, s51, 0x2000
	s_add_u32 s52, s24, 0x4000
	v_lshl_add_u64 v[180:181], s[24:25], 0, v[162:163]
	s_addc_u32 s53, s25, 0
	s_add_i32 s51, s40, s21
	global_load_lds_dwordx4 v[180:181], off
	v_lshl_add_u64 v[182:183], s[52:53], 0, v[166:167]
	s_mov_b32 m0, s51
	v_lshl_add_u64 v[184:185], s[26:27], 0, v[164:165]
	global_load_lds_dwordx4 v[182:183], off
	v_lshl_add_u64 v[182:183], s[52:53], 0, v[162:163]
	s_add_i32 m0, s51, 0x2000
	s_nop 0
	global_load_lds_dwordx4 v[182:183], off
	v_lshl_add_u64 v[182:183], s[26:27], 0, v[168:169]
	s_mov_b32 m0, s28
	s_nop 0
	global_load_lds_dwordx4 v[182:183], off
	s_mov_b32 m0, s29
	s_nop 0
	global_load_lds_dwordx4 v[184:185], off
	s_waitcnt vmcnt(8)
	s_waitcnt lgkmcnt(0)
	s_barrier
	s_setprio 1
	s_nop 3
	s_waitcnt lgkmcnt(0)
	v_mfma_scale_f32_16x16x128_f8f6f4 v[94:97], v[26:33], v[194:201], v[94:97], v191, v192 op_sel_hi:[0,0,0]
	v_mfma_scale_f32_16x16x128_f8f6f4 v[90:93], v[18:25], v[194:201], v[90:93], v191, v192 op_sel_hi:[0,0,0]
	v_mfma_scale_f32_16x16x128_f8f6f4 v[78:81], v[26:33], v[202:209], v[78:81], v191, v192 op_sel_hi:[0,0,0]
	v_mfma_scale_f32_16x16x128_f8f6f4 v[74:77], v[18:25], v[202:209], v[74:77], v191, v192 op_sel_hi:[0,0,0]
	v_mfma_scale_f32_16x16x128_f8f6f4 v[62:65], v[26:33], v[210:217], v[62:65], v191, v192 op_sel_hi:[0,0,0]
	v_mfma_scale_f32_16x16x128_f8f6f4 v[58:61], v[18:25], v[210:217], v[58:61], v191, v192 op_sel_hi:[0,0,0]
	v_mfma_scale_f32_16x16x128_f8f6f4 v[46:49], v[26:33], v[218:225], v[46:49], v191, v192 op_sel_hi:[0,0,0]
	v_mfma_scale_f32_16x16x128_f8f6f4 v[42:45], v[18:25], v[218:225], v[42:45], v191, v192 op_sel_hi:[0,0,0]
	s_setprio 0
	s_setprio 1
	s_nop 3
	v_mfma_scale_f32_16x16x128_f8f6f4 v[86:89], v[10:17], v[194:201], v[86:89], v191, v192 op_sel_hi:[0,0,0]
	v_mfma_scale_f32_16x16x128_f8f6f4 v[82:85], v[2:9], v[194:201], v[82:85], v191, v192 op_sel_hi:[0,0,0]
	v_mfma_scale_f32_16x16x128_f8f6f4 v[70:73], v[10:17], v[202:209], v[70:73], v191, v192 op_sel_hi:[0,0,0]
	v_mfma_scale_f32_16x16x128_f8f6f4 v[66:69], v[2:9], v[202:209], v[66:69], v191, v192 op_sel_hi:[0,0,0]
	v_mfma_scale_f32_16x16x128_f8f6f4 v[54:57], v[10:17], v[210:217], v[54:57], v191, v192 op_sel_hi:[0,0,0]
	v_mfma_scale_f32_16x16x128_f8f6f4 v[50:53], v[2:9], v[210:217], v[50:53], v191, v192 op_sel_hi:[0,0,0]
	v_mfma_scale_f32_16x16x128_f8f6f4 v[38:41], v[10:17], v[218:225], v[38:41], v191, v192 op_sel_hi:[0,0,0]
	v_mfma_scale_f32_16x16x128_f8f6f4 v[34:37], v[2:9], v[218:225], v[34:37], v191, v192 op_sel_hi:[0,0,0]
	s_setprio 0
	s_barrier
; #define PG8_STAGE(bufoff, gbase, voff) do { _Pragma("unroll") for (int _i = 0; _i < 2; ++_i) \
;         __builtin_amdgcn_global_load_lds((const unsigned*)((const char*)(gbase) + (voff)[_i]), (PG8_LAS unsigned*)(lds + (bufoff) + ldsw + _i * 8192), 16, 0, 0); } while (0)
; #define PG8_STAGE_A(bufoff, gbase, h, nx) do { if constexpr (Sched::GATHER) { const unsigned vv_[2] = {(nx) ? vAn[h][0] : vA[h][0], (nx) ? vAn[h][1] : vA[h][1]}; PG8_STAGE(bufoff, gbase, vv_); } \
;         else { PG8_STAGE(bufoff, (gbase) + (h) * hstep, voffA); } } while (0)
; #define PG8_LDA(dst, b, h) do { _Pragma("unroll") for (int m = 0; m < 4; ++m) _Pragma("unroll") for (int k = 0; k < 2; ++k) dst[m][k] = *(const PG8_LAS bf16x8*)(lds + PG8_SA(b, h) + aoff + m * 2048 + k * 1024); } while (0)
; #define PG8_LDB(dst, b, h) do { _Pragma("unroll") for (int n = 0; n < 2; ++n) _Pragma("unroll") for (int k = 0; k < 2; ++k) dst[n][k] = *(const PG8_LAS bf16x8*)(lds + PG8_SB(b, h) + boff + n * 2048 + k * 1024); } while (0)
; #define PG8_WAIT_V(n) asm volatile("s_waitcnt vmcnt(" #n ")" ::: "memory")
; #define PG8_WAIT_L(n) asm volatile("s_waitcnt lgkmcnt(" #n ")" ::: "memory")
; #define PG8_BAR __builtin_amdgcn_s_barrier()
; #define PG8_SCHED __builtin_amdgcn_sched_barrier(0)
;     ...
;             PG8_LDB(B0, 1, 0); PG8_LDB(B1, 1, 1); PG8_SCHED; PG8_LDA(At, 1, 0); PG8_STAGE_A(PG8_SA(0, 1), a2, 1, last);
;             PG8_WAIT_V(8); PG8_WAIT_L(0); PG8_BAR; PG8_MMA(0, 0, At, B0); PG8_MMA(0, 1, At, B1); PG8_BAR; PG8_SCHED;
;             PG8_LDA(At, 1, 1); PG8_STAGE(PG8_SB(1, 0), b3, voffB); PG8_STAGE(PG8_SB(1, 1), b3 + hstepB, voffB); PG8_STAGE_A(PG8_SA(1, 0), a3, 0, last);
;             PG8_WAIT_V(8); PG8_WAIT_L(0); PG8_BAR; PG8_MMA(1, 0, At, B0); PG8_MMA(1, 1, At, B1); PG8_BAR; PG8_SCHED;
;     __device__ __forceinline__ void operator()(const f32x4 (&acc)[2][2][4][2], const Unit& u, int wr, int wc, int fr, int fq) const {
;     ...
;             for (int m = 0; m < 4; ++m) { const int row = row0 + ai * HALF + m * 16; const float gt = gate[row] * YSCALE; unsigned char* rowp = O + (size_t)row * ldc + col0;
	s_add_i32 s51, 0, 0x18000
	s_add_i32 s52, 0, 0x1c000
	v_add_u32_e32 v14, s51, v186
	v_add_u32_e32 v30, s52, v186
	ds_read_b128 v[2:5], v14
	ds_read_b128 v[6:9], v14 offset:1024
	ds_read_b128 v[10:13], v14 offset:2048
	ds_read_b128 v[14:17], v14 offset:3072
	ds_read_b128 v[18:21], v30
	ds_read_b128 v[22:25], v30 offset:1024
	ds_read_b128 v[26:29], v30 offset:2048
	ds_read_b128 v[30:33], v30 offset:3072
	s_add_u32 s26, s26, 0x40000
	s_addc_u32 s27, s27, 0
	s_mov_b32 m0, s30
	v_lshl_add_u64 v[226:227], s[26:27], 0, v[168:169]
	ds_read_b128 v[194:197], v190 offset:32768
	ds_read_b128 v[198:201], v190 offset:33792
	ds_read_b128 v[202:205], v190 offset:34816
	ds_read_b128 v[206:209], v190 offset:35840
	ds_read_b128 v[210:213], v190 offset:36864
	ds_read_b128 v[214:217], v190 offset:37888
	ds_read_b128 v[218:221], v190 offset:38912
	ds_read_b128 v[222:225], v190 offset:39936
	global_load_lds_dwordx4 v[226:227], off
	v_lshl_add_u64 v[226:227], s[26:27], 0, v[164:165]
	s_mov_b32 m0, s31
	s_nop 0
	global_load_lds_dwordx4 v[226:227], off
	s_waitcnt vmcnt(8)
	s_waitcnt lgkmcnt(0)
	s_barrier
	s_setprio 1
	s_nop 3
	s_waitcnt lgkmcnt(0)
	v_mfma_scale_f32_16x16x128_f8f6f4 v[158:161], v[2:9], v[194:201], v[158:161], v191, v192 op_sel_hi:[0,0,0]
	v_mfma_scale_f32_16x16x128_f8f6f4 v[154:157], v[10:17], v[194:201], v[154:157], v191, v192 op_sel_hi:[0,0,0]
	v_mfma_scale_f32_16x16x128_f8f6f4 v[142:145], v[2:9], v[202:209], v[142:145], v191, v192 op_sel_hi:[0,0,0]
	v_mfma_scale_f32_16x16x128_f8f6f4 v[138:141], v[10:17], v[202:209], v[138:141], v191, v192 op_sel_hi:[0,0,0]
	v_mfma_scale_f32_16x16x128_f8f6f4 v[126:129], v[2:9], v[210:217], v[126:129], v191, v192 op_sel_hi:[0,0,0]
	v_mfma_scale_f32_16x16x128_f8f6f4 v[122:125], v[10:17], v[210:217], v[122:125], v191, v192 op_sel_hi:[0,0,0]
	v_mfma_scale_f32_16x16x128_f8f6f4 v[110:113], v[2:9], v[218:225], v[110:113], v191, v192 op_sel_hi:[0,0,0]
	v_mfma_scale_f32_16x16x128_f8f6f4 v[106:109], v[10:17], v[218:225], v[106:109], v191, v192 op_sel_hi:[0,0,0]
	s_setprio 0
	s_setprio 1
	s_nop 3
	v_mfma_scale_f32_16x16x128_f8f6f4 v[150:153], v[18:25], v[194:201], v[150:153], v191, v192 op_sel_hi:[0,0,0]
	v_mfma_scale_f32_16x16x128_f8f6f4 v[146:149], v[26:33], v[194:201], v[146:149], v191, v192 op_sel_hi:[0,0,0]
	v_mfma_scale_f32_16x16x128_f8f6f4 v[134:137], v[18:25], v[202:209], v[134:137], v191, v192 op_sel_hi:[0,0,0]
	v_mfma_scale_f32_16x16x128_f8f6f4 v[130:133], v[26:33], v[202:209], v[130:133], v191, v192 op_sel_hi:[0,0,0]
	v_mfma_scale_f32_16x16x128_f8f6f4 v[118:121], v[18:25], v[210:217], v[118:121], v191, v192 op_sel_hi:[0,0,0]
	v_mfma_scale_f32_16x16x128_f8f6f4 v[114:117], v[26:33], v[210:217], v[114:117], v191, v192 op_sel_hi:[0,0,0]
	v_mfma_scale_f32_16x16x128_f8f6f4 v[102:105], v[18:25], v[218:225], v[102:105], v191, v192 op_sel_hi:[0,0,0]
	v_mfma_scale_f32_16x16x128_f8f6f4 v[98:101], v[26:33], v[218:225], v[98:101], v191, v192 op_sel_hi:[0,0,0]
	s_setprio 0
	s_barrier
	s_add_i32 s26, s51, s21
	v_lshl_add_u64 v[178:179], v[178:179], 0, s[8:9]
	s_mov_b32 m0, s26
	ds_read_b128 v[194:197], v190 offset:49152
	ds_read_b128 v[198:201], v190 offset:50176
	ds_read_b128 v[202:205], v190 offset:51200
	ds_read_b128 v[206:209], v190 offset:52224
	ds_read_b128 v[210:213], v190 offset:53248
	ds_read_b128 v[214:217], v190 offset:54272
	ds_read_b128 v[218:221], v190 offset:55296
	ds_read_b128 v[222:225], v190 offset:56320
	global_load_lds_dwordx4 v[178:179], off
	s_add_i32 m0, s26, 0x2000
	s_add_u32 s24, s24, 0x4080
	v_lshl_add_u64 v[178:179], v[180:181], 0, s[8:9]
	s_addc_u32 s25, s25, 0
	s_add_i32 s26, s52, s21
	global_load_lds_dwordx4 v[178:179], off
	v_lshl_add_u64 v[178:179], s[24:25], 0, v[166:167]
	s_mov_b32 m0, s26
	s_nop 0
	global_load_lds_dwordx4 v[178:179], off
	v_lshl_add_u64 v[178:179], s[24:25], 0, v[162:163]
	s_add_i32 m0, s26, 0x2000
	s_nop 0
	global_load_lds_dwordx4 v[178:179], off
	v_lshl_add_u64 v[178:179], v[182:183], 0, s[8:9]
	s_mov_b32 m0, s36
	s_nop 0
	global_load_lds_dwordx4 v[178:179], off
	v_lshl_add_u64 v[178:179], v[184:185], 0, s[8:9]
	s_mov_b32 m0, s37
	s_nop 0
	global_load_lds_dwordx4 v[178:179], off
	s_waitcnt vmcnt(8)
	s_cmp_eq_u32 s50, 12
	s_cbranch_scc0 .Lgate19_skip
	v_lshl_add_u32 v236, s20, 8, v1
	v_ashrrev_i32_e32 v237, 31, v236
	v_lshl_add_u64 v[236:237], v[236:237], 2, s[0:1]
	global_load_dword v228, v[236:237], off
	global_load_dword v229, v[236:237], off offset:64
	global_load_dword v230, v[236:237], off offset:128
	global_load_dword v231, v[236:237], off offset:192
	global_load_dword v232, v[236:237], off offset:512
	global_load_dword v233, v[236:237], off offset:576
	global_load_dword v234, v[236:237], off offset:640
	global_load_dword v235, v[236:237], off offset:704
; #define PG8_WAIT_V(n) asm volatile("s_waitcnt vmcnt(" #n ")" ::: "memory")
; #define PG8_WAIT_L(n) asm volatile("s_waitcnt lgkmcnt(" #n ")" ::: "memory")
; #define PG8_BAR __builtin_amdgcn_s_barrier()
; #define PG8_SCHED __builtin_amdgcn_sched_barrier(0)
; __device__ __forceinline__ unsigned pk4_fp8(float a, float b, float c, float d) { unsigned w = 0u; w = __builtin_amdgcn_cvt_pk_fp8_f32(a, b, w, false); w = __builtin_amdgcn_cvt_pk_fp8_f32(c, d, w, true); return w; }
; __device__ __forceinline__ float clamp448(float v) { return __builtin_amdgcn_fmed3f(v, -448.f, 448.f); }
;     ...
;             PG8_WAIT_V(8); PG8_WAIT_L(0); PG8_BAR; PG8_MMA(1, 0, At, B0); PG8_MMA(1, 1, At, B1); PG8_BAR; PG8_SCHED;
;     __device__ __forceinline__ void operator()(const f32x4 (&acc)[2][2][4][2], const Unit& u, int wr, int wc, int fr, int fq) const {
;         const int row0 = u.pm * BM + wr * 64 + fr, col0 = u.pn * BM + wc * 64 + 16 * fq;
; #pragma unroll
;         for (int ai = 0; ai < 2; ++ai)
; #pragma unroll
;             for (int m = 0; m < 4; ++m) { const int row = row0 + ai * HALF + m * 16; const float gt = gate[row] * YSCALE; unsigned char* rowp = O + (size_t)row * ldc + col0;
;                 unsigned w[4];
; #pragma unroll
;                 for (int bj = 0; bj < 2; ++bj)
; #pragma unroll
;                     for (int n = 0; n < 2; ++n) { const f32x4 v = acc[ai][bj][m][n] * gt; w[2 * bj + n] = pk4_fp8(clamp448(v[0]), clamp448(v[1]), clamp448(v[2]), clamp448(v[3])); }
;                 *(u32x4*)rowp = (u32x4){w[0], w[1], w[2], w[3]}; }
.Lgate19_skip:
	s_waitcnt lgkmcnt(0)
	s_barrier
	s_setprio 1
	s_nop 3
	s_waitcnt lgkmcnt(0)
	v_mfma_scale_f32_16x16x128_f8f6f4 v[94:97], v[2:9], v[194:201], v[94:97], v191, v192 op_sel_hi:[0,0,0]
	v_mfma_scale_f32_16x16x128_f8f6f4 v[90:93], v[10:17], v[194:201], v[90:93], v191, v192 op_sel_hi:[0,0,0]
	v_mfma_scale_f32_16x16x128_f8f6f4 v[78:81], v[2:9], v[202:209], v[78:81], v191, v192 op_sel_hi:[0,0,0]
	v_mfma_scale_f32_16x16x128_f8f6f4 v[74:77], v[10:17], v[202:209], v[74:77], v191, v192 op_sel_hi:[0,0,0]
	v_mfma_scale_f32_16x16x128_f8f6f4 v[62:65], v[2:9], v[210:217], v[62:65], v191, v192 op_sel_hi:[0,0,0]
	v_mfma_scale_f32_16x16x128_f8f6f4 v[58:61], v[10:17], v[210:217], v[58:61], v191, v192 op_sel_hi:[0,0,0]
	v_mfma_scale_f32_16x16x128_f8f6f4 v[46:49], v[2:9], v[218:225], v[46:49], v191, v192 op_sel_hi:[0,0,0]
	v_mfma_scale_f32_16x16x128_f8f6f4 v[42:45], v[10:17], v[218:225], v[42:45], v191, v192 op_sel_hi:[0,0,0]
	s_setprio 0
	s_setprio 1
	s_nop 3
	v_mfma_scale_f32_16x16x128_f8f6f4 v[86:89], v[18:25], v[194:201], v[86:89], v191, v192 op_sel_hi:[0,0,0]
	v_mfma_scale_f32_16x16x128_f8f6f4 v[82:85], v[26:33], v[194:201], v[82:85], v191, v192 op_sel_hi:[0,0,0]
	v_mfma_scale_f32_16x16x128_f8f6f4 v[70:73], v[18:25], v[202:209], v[70:73], v191, v192 op_sel_hi:[0,0,0]
	v_mfma_scale_f32_16x16x128_f8f6f4 v[66:69], v[26:33], v[202:209], v[66:69], v191, v192 op_sel_hi:[0,0,0]
	v_mfma_scale_f32_16x16x128_f8f6f4 v[54:57], v[18:25], v[210:217], v[54:57], v191, v192 op_sel_hi:[0,0,0]
	v_mfma_scale_f32_16x16x128_f8f6f4 v[50:53], v[26:33], v[210:217], v[50:53], v191, v192 op_sel_hi:[0,0,0]
	v_mfma_scale_f32_16x16x128_f8f6f4 v[38:41], v[18:25], v[218:225], v[38:41], v191, v192 op_sel_hi:[0,0,0]
	v_mfma_scale_f32_16x16x128_f8f6f4 v[34:37], v[26:33], v[218:225], v[34:37], v191, v192 op_sel_hi:[0,0,0]
	s_setprio 0
	s_barrier
	s_add_i32 s50, s50, 2
	s_add_u32 s22, s22, 0x100
	s_addc_u32 s23, s23, 0
	s_add_u32 s48, s48, 0x100
	s_addc_u32 s49, s49, 0
	s_cmp_gt_u32 s50, 13
	s_cbranch_scc0 .LBB0_1626
	s_and_b64 vcc, exec, s[10:11]
	s_cbranch_vccz .LBB0_1629
	s_barrier
.LBB0_1629:
	v_lshl_add_u32 v8, s20, 8, v1
	v_ashrrev_i32_e32 v9, 31, v8
	v_lshl_add_u64 v[2:3], v[8:9], 2, s[0:1]
	v_mov_b32_e32 v10, 0
	v_mov_b32_e32 v11, 0
	v_mov_b32_e32 v12, 0
	v_mov_b32_e32 v13, 0
	v_lshlrev_b64 v[4:5], 10, v[8:9]
	v_lshl_or_b32 v6, s33, 8, v187
	v_ashrrev_i32_e32 v7, 31, v6
	v_or_b32_e32 v14, 16, v8
	v_lshl_add_u64 v[4:5], s[94:95], 0, v[4:5]
	v_ashrrev_i32_e32 v15, 31, v14
	v_lshl_add_u64 v[4:5], v[4:5], 0, v[6:7]
	s_waitcnt vmcnt(0)
	v_mul_f32_e32 v16, 0x42000000, v228
	v_pk_mul_f32 v[18:19], v[160:161], v[16:17] op_sel_hi:[1,0]
	v_pk_mul_f32 v[20:21], v[158:159], v[16:17] op_sel_hi:[1,0]
	v_pk_mul_f32 v[22:23], v[156:157], v[16:17] op_sel_hi:[1,0]
	v_pk_mul_f32 v[24:25], v[154:155], v[16:17] op_sel_hi:[1,0]
	v_pk_mul_f32 v[26:27], v[152:153], v[16:17] op_sel_hi:[1,0]
	v_pk_mul_f32 v[28:29], v[150:151], v[16:17] op_sel_hi:[1,0]
	v_pk_mul_f32 v[30:31], v[148:149], v[16:17] op_sel_hi:[1,0]
	v_pk_mul_f32 v[16:17], v[146:147], v[16:17] op_sel_hi:[1,0]
	v_med3_f32 v9, v20, s41, v193
	v_med3_f32 v20, v21, s41, v193
	v_med3_f32 v21, v24, s41, v193
	v_med3_f32 v24, v25, s41, v193
	v_med3_f32 v25, v28, s41, v193
	v_med3_f32 v28, v29, s41, v193
	v_med3_f32 v16, v16, s41, v193
	v_med3_f32 v17, v17, s41, v193
	v_cvt_pk_fp8_f32 v10, v9, v20
	v_cvt_pk_fp8_f32 v11, v21, v24
	v_cvt_pk_fp8_f32 v12, v25, v28
	v_cvt_pk_fp8_f32 v13, v16, v17
	v_med3_f32 v18, v18, s41, v193
	v_med3_f32 v19, v19, s41, v193
	v_med3_f32 v22, v22, s41, v193
	v_med3_f32 v23, v23, s41, v193
	v_med3_f32 v26, v26, s41, v193
	v_med3_f32 v27, v27, s41, v193
	v_med3_f32 v29, v30, s41, v193
	v_med3_f32 v30, v31, s41, v193
	v_cvt_pk_fp8_f32 v10, v18, v19 op_sel:[0,0,1]
	v_cvt_pk_fp8_f32 v11, v22, v23 op_sel:[0,0,1]
	v_cvt_pk_fp8_f32 v12, v26, v27 op_sel:[0,0,1]
	v_cvt_pk_fp8_f32 v13, v29, v30 op_sel:[0,0,1]
	v_lshl_add_u64 v[16:17], v[14:15], 2, s[0:1]
	v_lshlrev_b64 v[14:15], 10, v[14:15]
	v_lshl_add_u64 v[14:15], s[94:95], 0, v[14:15]
	global_store_dwordx4 v[4:5], v[10:13], off
	s_nop 1
	v_or_b32_e32 v16, 32, v8
	v_mov_b32_e32 v10, 0
	v_mov_b32_e32 v11, 0
	v_mov_b32_e32 v12, 0
	v_mov_b32_e32 v13, 0
	v_ashrrev_i32_e32 v17, 31, v16
	v_lshl_add_u64 v[14:15], v[14:15], 0, v[6:7]
	v_mul_f32_e32 v18, 0x42000000, v229
	v_pk_mul_f32 v[20:21], v[144:145], v[18:19] op_sel_hi:[1,0]
	v_pk_mul_f32 v[22:23], v[142:143], v[18:19] op_sel_hi:[1,0]
	v_pk_mul_f32 v[24:25], v[140:141], v[18:19] op_sel_hi:[1,0]
	v_pk_mul_f32 v[26:27], v[138:139], v[18:19] op_sel_hi:[1,0]
	v_pk_mul_f32 v[28:29], v[136:137], v[18:19] op_sel_hi:[1,0]
	v_pk_mul_f32 v[30:31], v[134:135], v[18:19] op_sel_hi:[1,0]
	v_pk_mul_f32 v[32:33], v[132:133], v[18:19] op_sel_hi:[1,0]
	v_pk_mul_f32 v[18:19], v[130:131], v[18:19] op_sel_hi:[1,0]
	v_med3_f32 v9, v22, s41, v193
	v_med3_f32 v22, v23, s41, v193
	v_med3_f32 v23, v26, s41, v193
	v_med3_f32 v26, v27, s41, v193
	v_med3_f32 v27, v30, s41, v193
	v_med3_f32 v30, v31, s41, v193
	v_med3_f32 v18, v18, s41, v193
	v_med3_f32 v19, v19, s41, v193
	v_cvt_pk_fp8_f32 v10, v9, v22
	v_cvt_pk_fp8_f32 v11, v23, v26
	v_cvt_pk_fp8_f32 v12, v27, v30
	v_cvt_pk_fp8_f32 v13, v18, v19
	v_med3_f32 v20, v20, s41, v193
	v_med3_f32 v21, v21, s41, v193
	v_med3_f32 v24, v24, s41, v193
	v_med3_f32 v25, v25, s41, v193
	v_med3_f32 v28, v28, s41, v193
	v_med3_f32 v29, v29, s41, v193
	v_med3_f32 v31, v32, s41, v193
	v_med3_f32 v32, v33, s41, v193
	v_cvt_pk_fp8_f32 v10, v20, v21 op_sel:[0,0,1]
	v_cvt_pk_fp8_f32 v11, v24, v25 op_sel:[0,0,1]
	v_cvt_pk_fp8_f32 v12, v28, v29 op_sel:[0,0,1]
	v_cvt_pk_fp8_f32 v13, v31, v32 op_sel:[0,0,1]
; __device__ __forceinline__ unsigned pk4_fp8(float a, float b, float c, float d) { unsigned w = 0u; w = __builtin_amdgcn_cvt_pk_fp8_f32(a, b, w, false); w = __builtin_amdgcn_cvt_pk_fp8_f32(c, d, w, true); return w; }
; __device__ __forceinline__ float clamp448(float v) { return __builtin_amdgcn_fmed3f(v, -448.f, 448.f); }
;     __device__ __forceinline__ void operator()(const f32x4 (&acc)[2][2][4][2], const Unit& u, int wr, int wc, int fr, int fq) const {
;     ...
; #pragma unroll
;         for (int ai = 0; ai < 2; ++ai)
; #pragma unroll
;             for (int m = 0; m < 4; ++m) { const int row = row0 + ai * HALF + m * 16; const float gt = gate[row] * YSCALE; unsigned char* rowp = O + (size_t)row * ldc + col0;
;                 unsigned w[4];
; #pragma unroll
;                 for (int bj = 0; bj < 2; ++bj)
; #pragma unroll
;                     for (int n = 0; n < 2; ++n) { const f32x4 v = acc[ai][bj][m][n] * gt; w[2 * bj + n] = pk4_fp8(clamp448(v[0]), clamp448(v[1]), clamp448(v[2]), clamp448(v[3])); }
;                 *(u32x4*)rowp = (u32x4){w[0], w[1], w[2], w[3]}; }
	v_lshl_add_u64 v[18:19], v[16:17], 2, s[0:1]
	global_store_dwordx4 v[14:15], v[10:13], off
	s_nop 1
	v_or_b32_e32 v14, 48, v8
	v_lshlrev_b64 v[8:9], 10, v[16:17]
	v_mov_b32_e32 v10, 0
	v_mov_b32_e32 v11, 0
	v_mov_b32_e32 v12, 0
	v_mov_b32_e32 v13, 0
	v_lshl_add_u64 v[8:9], s[94:95], 0, v[8:9]
	v_ashrrev_i32_e32 v15, 31, v14
	v_lshl_add_u64 v[8:9], v[8:9], 0, v[6:7]
	v_mul_f32_e32 v16, 0x42000000, v230
	v_pk_mul_f32 v[18:19], v[128:129], v[16:17] op_sel_hi:[1,0]
	v_pk_mul_f32 v[20:21], v[126:127], v[16:17] op_sel_hi:[1,0]
	v_pk_mul_f32 v[22:23], v[124:125], v[16:17] op_sel_hi:[1,0]
	v_pk_mul_f32 v[24:25], v[122:123], v[16:17] op_sel_hi:[1,0]
	v_pk_mul_f32 v[26:27], v[120:121], v[16:17] op_sel_hi:[1,0]
	v_pk_mul_f32 v[28:29], v[118:119], v[16:17] op_sel_hi:[1,0]
	v_pk_mul_f32 v[30:31], v[116:117], v[16:17] op_sel_hi:[1,0]
	v_pk_mul_f32 v[16:17], v[114:115], v[16:17] op_sel_hi:[1,0]
	v_med3_f32 v20, v20, s41, v193
	v_med3_f32 v21, v21, s41, v193
	v_med3_f32 v24, v24, s41, v193
	v_med3_f32 v25, v25, s41, v193
	v_med3_f32 v28, v28, s41, v193
	v_med3_f32 v29, v29, s41, v193
	v_med3_f32 v16, v16, s41, v193
	v_med3_f32 v17, v17, s41, v193
	v_cvt_pk_fp8_f32 v10, v20, v21
	v_cvt_pk_fp8_f32 v11, v24, v25
	v_cvt_pk_fp8_f32 v12, v28, v29
	v_cvt_pk_fp8_f32 v13, v16, v17
	v_med3_f32 v18, v18, s41, v193
	v_med3_f32 v19, v19, s41, v193
	v_med3_f32 v22, v22, s41, v193
	v_med3_f32 v23, v23, s41, v193
	v_med3_f32 v26, v26, s41, v193
	v_med3_f32 v27, v27, s41, v193
	v_med3_f32 v30, v30, s41, v193
	v_med3_f32 v31, v31, s41, v193
	v_cvt_pk_fp8_f32 v10, v18, v19 op_sel:[0,0,1]
	v_cvt_pk_fp8_f32 v11, v22, v23 op_sel:[0,0,1]
	v_cvt_pk_fp8_f32 v12, v26, v27 op_sel:[0,0,1]
	v_cvt_pk_fp8_f32 v13, v30, v31 op_sel:[0,0,1]
	v_lshl_add_u64 v[16:17], v[14:15], 2, s[0:1]
	global_store_dwordx4 v[8:9], v[10:13], off
	s_nop 1
	v_mov_b32_e32 v8, 0
	v_mov_b32_e32 v9, 0
	v_mov_b32_e32 v10, 0
	v_mov_b32_e32 v11, 0
	v_mul_f32_e32 v12, 0x42000000, v231
	v_pk_mul_f32 v[16:17], v[112:113], v[12:13] op_sel_hi:[1,0]
	v_pk_mul_f32 v[18:19], v[110:111], v[12:13] op_sel_hi:[1,0]
	v_pk_mul_f32 v[20:21], v[108:109], v[12:13] op_sel_hi:[1,0]
	v_pk_mul_f32 v[22:23], v[106:107], v[12:13] op_sel_hi:[1,0]
	v_pk_mul_f32 v[24:25], v[104:105], v[12:13] op_sel_hi:[1,0]
	v_pk_mul_f32 v[26:27], v[102:103], v[12:13] op_sel_hi:[1,0]
	v_pk_mul_f32 v[28:29], v[100:101], v[12:13] op_sel_hi:[1,0]
	v_pk_mul_f32 v[12:13], v[98:99], v[12:13] op_sel_hi:[1,0]
	v_med3_f32 v18, v18, s41, v193
	v_med3_f32 v19, v19, s41, v193
	v_med3_f32 v22, v22, s41, v193
	v_med3_f32 v23, v23, s41, v193
	v_med3_f32 v26, v26, s41, v193
	v_med3_f32 v27, v27, s41, v193
	v_med3_f32 v12, v12, s41, v193
	v_med3_f32 v13, v13, s41, v193
	v_cvt_pk_fp8_f32 v8, v18, v19
	v_cvt_pk_fp8_f32 v9, v22, v23
	v_cvt_pk_fp8_f32 v10, v26, v27
	v_cvt_pk_fp8_f32 v11, v12, v13
	v_med3_f32 v16, v16, s41, v193
	v_med3_f32 v17, v17, s41, v193
	v_med3_f32 v20, v20, s41, v193
	v_med3_f32 v21, v21, s41, v193
	v_med3_f32 v24, v24, s41, v193
	v_med3_f32 v25, v25, s41, v193
	v_med3_f32 v28, v28, s41, v193
	v_med3_f32 v29, v29, s41, v193
	v_cvt_pk_fp8_f32 v8, v16, v17 op_sel:[0,0,1]
	v_cvt_pk_fp8_f32 v9, v20, v21 op_sel:[0,0,1]
	v_cvt_pk_fp8_f32 v10, v24, v25 op_sel:[0,0,1]
	v_cvt_pk_fp8_f32 v11, v28, v29 op_sel:[0,0,1]
	v_lshlrev_b64 v[12:13], 10, v[14:15]
	v_lshl_add_u64 v[12:13], s[94:95], 0, v[12:13]
	v_lshl_add_u64 v[6:7], v[12:13], 0, v[6:7]
	global_store_dwordx4 v[6:7], v[8:11], off
	s_nop 1
	v_mov_b32_e32 v6, 0
	v_mov_b32_e32 v7, 0
	v_mov_b32_e32 v8, 0
	v_mov_b32_e32 v9, 0
	v_mul_f32_e32 v10, 0x42000000, v232
	v_pk_mul_f32 v[12:13], v[96:97], v[10:11] op_sel_hi:[1,0]
	v_pk_mul_f32 v[14:15], v[94:95], v[10:11] op_sel_hi:[1,0]
	v_pk_mul_f32 v[16:17], v[92:93], v[10:11] op_sel_hi:[1,0]
	v_pk_mul_f32 v[18:19], v[90:91], v[10:11] op_sel_hi:[1,0]
	v_pk_mul_f32 v[20:21], v[88:89], v[10:11] op_sel_hi:[1,0]
	v_pk_mul_f32 v[22:23], v[86:87], v[10:11] op_sel_hi:[1,0]
	v_pk_mul_f32 v[24:25], v[84:85], v[10:11] op_sel_hi:[1,0]
	v_pk_mul_f32 v[10:11], v[82:83], v[10:11] op_sel_hi:[1,0]
	v_med3_f32 v14, v14, s41, v193
	v_med3_f32 v15, v15, s41, v193
	v_med3_f32 v18, v18, s41, v193
	v_med3_f32 v19, v19, s41, v193
	v_med3_f32 v22, v22, s41, v193
	v_med3_f32 v23, v23, s41, v193
	v_med3_f32 v10, v10, s41, v193
	v_med3_f32 v11, v11, s41, v193
	v_cvt_pk_fp8_f32 v6, v14, v15
	v_cvt_pk_fp8_f32 v7, v18, v19
	v_cvt_pk_fp8_f32 v8, v22, v23
	v_cvt_pk_fp8_f32 v9, v10, v11
	v_med3_f32 v12, v12, s41, v193
	v_med3_f32 v13, v13, s41, v193
	v_med3_f32 v16, v16, s41, v193
	v_med3_f32 v17, v17, s41, v193
	v_med3_f32 v20, v20, s41, v193
	v_med3_f32 v21, v21, s41, v193
	v_med3_f32 v24, v24, s41, v193
	v_med3_f32 v25, v25, s41, v193
	v_cvt_pk_fp8_f32 v6, v12, v13 op_sel:[0,0,1]
	v_cvt_pk_fp8_f32 v7, v16, v17 op_sel:[0,0,1]
	v_cvt_pk_fp8_f32 v8, v20, v21 op_sel:[0,0,1]
	v_cvt_pk_fp8_f32 v9, v24, v25 op_sel:[0,0,1]
	v_add_co_u32_e32 v10, vcc, s42, v4
; __device__ __forceinline__ unsigned pk4_fp8(float a, float b, float c, float d) { unsigned w = 0u; w = __builtin_amdgcn_cvt_pk_fp8_f32(a, b, w, false); w = __builtin_amdgcn_cvt_pk_fp8_f32(c, d, w, true); return w; }
; __device__ __forceinline__ float clamp448(float v) { return __builtin_amdgcn_fmed3f(v, -448.f, 448.f); }
;     __device__ __forceinline__ void operator()(const f32x4 (&acc)[2][2][4][2], const Unit& u, int wr, int wc, int fr, int fq) const {
;     ...
; #pragma unroll
;         for (int ai = 0; ai < 2; ++ai)
; #pragma unroll
;             for (int m = 0; m < 4; ++m) { const int row = row0 + ai * HALF + m * 16; const float gt = gate[row] * YSCALE; unsigned char* rowp = O + (size_t)row * ldc + col0;
;                 unsigned w[4];
; #pragma unroll
;                 for (int bj = 0; bj < 2; ++bj)
; #pragma unroll
;                     for (int n = 0; n < 2; ++n) { const f32x4 v = acc[ai][bj][m][n] * gt; w[2 * bj + n] = pk4_fp8(clamp448(v[0]), clamp448(v[1]), clamp448(v[2]), clamp448(v[3])); }
;                 *(u32x4*)rowp = (u32x4){w[0], w[1], w[2], w[3]}; }
	s_nop 1
	v_addc_co_u32_e32 v11, vcc, 0, v5, vcc
	global_store_dwordx4 v[10:11], v[6:9], off
	s_nop 1
	v_mul_f32_e32 v10, 0x42000000, v233
	v_pk_mul_f32 v[12:13], v[80:81], v[10:11] op_sel_hi:[1,0]
	v_pk_mul_f32 v[14:15], v[78:79], v[10:11] op_sel_hi:[1,0]
	v_pk_mul_f32 v[16:17], v[76:77], v[10:11] op_sel_hi:[1,0]
	v_pk_mul_f32 v[18:19], v[74:75], v[10:11] op_sel_hi:[1,0]
	v_pk_mul_f32 v[20:21], v[72:73], v[10:11] op_sel_hi:[1,0]
	v_pk_mul_f32 v[22:23], v[70:71], v[10:11] op_sel_hi:[1,0]
	v_pk_mul_f32 v[24:25], v[68:69], v[10:11] op_sel_hi:[1,0]
	v_pk_mul_f32 v[10:11], v[66:67], v[10:11] op_sel_hi:[1,0]
	v_mov_b32_e32 v6, 0
	v_mov_b32_e32 v7, 0
	v_mov_b32_e32 v8, 0
	v_mov_b32_e32 v9, 0
	v_med3_f32 v14, v14, s41, v193
	v_med3_f32 v15, v15, s41, v193
	v_med3_f32 v18, v18, s41, v193
	v_med3_f32 v19, v19, s41, v193
	v_med3_f32 v22, v22, s41, v193
	v_med3_f32 v23, v23, s41, v193
	v_med3_f32 v10, v10, s41, v193
	v_med3_f32 v11, v11, s41, v193
	v_cvt_pk_fp8_f32 v6, v14, v15
	v_cvt_pk_fp8_f32 v7, v18, v19
	v_cvt_pk_fp8_f32 v8, v22, v23
	v_cvt_pk_fp8_f32 v9, v10, v11
	v_med3_f32 v12, v12, s41, v193
	v_med3_f32 v13, v13, s41, v193
	v_med3_f32 v16, v16, s41, v193
	v_med3_f32 v17, v17, s41, v193
	v_med3_f32 v20, v20, s41, v193
	v_med3_f32 v21, v21, s41, v193
	v_med3_f32 v24, v24, s41, v193
	v_med3_f32 v25, v25, s41, v193
	v_cvt_pk_fp8_f32 v6, v12, v13 op_sel:[0,0,1]
	v_cvt_pk_fp8_f32 v7, v16, v17 op_sel:[0,0,1]
	v_cvt_pk_fp8_f32 v8, v20, v21 op_sel:[0,0,1]
	v_cvt_pk_fp8_f32 v9, v24, v25 op_sel:[0,0,1]
	v_add_co_u32_e32 v10, vcc, s43, v4
	s_nop 1
	v_addc_co_u32_e32 v11, vcc, 0, v5, vcc
	global_store_dwordx4 v[10:11], v[6:9], off
	s_nop 1
	v_mul_f32_e32 v10, 0x42000000, v234
	v_pk_mul_f32 v[12:13], v[64:65], v[10:11] op_sel_hi:[1,0]
	v_pk_mul_f32 v[14:15], v[62:63], v[10:11] op_sel_hi:[1,0]
	v_pk_mul_f32 v[16:17], v[60:61], v[10:11] op_sel_hi:[1,0]
	v_pk_mul_f32 v[18:19], v[58:59], v[10:11] op_sel_hi:[1,0]
	v_pk_mul_f32 v[20:21], v[56:57], v[10:11] op_sel_hi:[1,0]
	v_pk_mul_f32 v[22:23], v[54:55], v[10:11] op_sel_hi:[1,0]
	v_pk_mul_f32 v[24:25], v[52:53], v[10:11] op_sel_hi:[1,0]
	v_pk_mul_f32 v[10:11], v[50:51], v[10:11] op_sel_hi:[1,0]
	v_mov_b32_e32 v6, 0
	v_mov_b32_e32 v7, 0
	v_mov_b32_e32 v8, 0
	v_mov_b32_e32 v9, 0
	v_med3_f32 v14, v14, s41, v193
	v_med3_f32 v15, v15, s41, v193
	v_med3_f32 v18, v18, s41, v193
	v_med3_f32 v19, v19, s41, v193
	v_med3_f32 v22, v22, s41, v193
	v_med3_f32 v23, v23, s41, v193
	v_med3_f32 v10, v10, s41, v193
	v_med3_f32 v11, v11, s41, v193
	v_cvt_pk_fp8_f32 v6, v14, v15
	v_cvt_pk_fp8_f32 v7, v18, v19
	v_cvt_pk_fp8_f32 v8, v22, v23
	v_cvt_pk_fp8_f32 v9, v10, v11
	v_med3_f32 v12, v12, s41, v193
	v_med3_f32 v13, v13, s41, v193
	v_med3_f32 v16, v16, s41, v193
	v_med3_f32 v17, v17, s41, v193
	v_med3_f32 v20, v20, s41, v193
	v_med3_f32 v21, v21, s41, v193
	v_med3_f32 v24, v24, s41, v193
	v_med3_f32 v25, v25, s41, v193
	v_cvt_pk_fp8_f32 v6, v12, v13 op_sel:[0,0,1]
	v_cvt_pk_fp8_f32 v7, v16, v17 op_sel:[0,0,1]
	v_cvt_pk_fp8_f32 v8, v20, v21 op_sel:[0,0,1]
	v_cvt_pk_fp8_f32 v9, v24, v25 op_sel:[0,0,1]
	v_add_co_u32_e32 v10, vcc, s44, v4
	s_nop 1
	v_addc_co_u32_e32 v11, vcc, 0, v5, vcc
	global_store_dwordx4 v[10:11], v[6:9], off
	s_nop 1
	v_add_co_u32_e32 v2, vcc, 0x2c000, v4
	v_mov_b32_e32 v6, 0
	v_mov_b32_e32 v7, 0
	v_mov_b32_e32 v8, 0
	v_mov_b32_e32 v9, 0
	v_mul_f32_e32 v4, 0x42000000, v235
	v_pk_mul_f32 v[12:13], v[46:47], v[4:5] op_sel_hi:[1,0]
	v_pk_mul_f32 v[16:17], v[42:43], v[4:5] op_sel_hi:[1,0]
	v_pk_mul_f32 v[20:21], v[38:39], v[4:5] op_sel_hi:[1,0]
	v_pk_mul_f32 v[24:25], v[34:35], v[4:5] op_sel_hi:[1,0]
	v_pk_mul_f32 v[10:11], v[48:49], v[4:5] op_sel_hi:[1,0]
	v_pk_mul_f32 v[14:15], v[44:45], v[4:5] op_sel_hi:[1,0]
	v_pk_mul_f32 v[18:19], v[40:41], v[4:5] op_sel_hi:[1,0]
	v_pk_mul_f32 v[22:23], v[36:37], v[4:5] op_sel_hi:[1,0]
	v_med3_f32 v3, v12, s41, v193
	v_med3_f32 v4, v13, s41, v193
	v_med3_f32 v12, v16, s41, v193
	v_med3_f32 v13, v17, s41, v193
	v_med3_f32 v16, v20, s41, v193
	v_med3_f32 v17, v21, s41, v193
	v_med3_f32 v20, v24, s41, v193
	v_med3_f32 v21, v25, s41, v193
	v_cvt_pk_fp8_f32 v6, v3, v4
	v_cvt_pk_fp8_f32 v7, v12, v13
	v_cvt_pk_fp8_f32 v8, v16, v17
	v_cvt_pk_fp8_f32 v9, v20, v21
	v_med3_f32 v10, v10, s41, v193
	v_med3_f32 v11, v11, s41, v193
	v_med3_f32 v14, v14, s41, v193
	v_med3_f32 v15, v15, s41, v193
	v_med3_f32 v18, v18, s41, v193
	v_med3_f32 v19, v19, s41, v193
	v_med3_f32 v22, v22, s41, v193
	v_med3_f32 v23, v23, s41, v193
	v_cvt_pk_fp8_f32 v6, v10, v11 op_sel:[0,0,1]
	v_cvt_pk_fp8_f32 v7, v14, v15 op_sel:[0,0,1]
	v_cvt_pk_fp8_f32 v8, v18, v19 op_sel:[0,0,1]
	v_cvt_pk_fp8_f32 v9, v22, v23 op_sel:[0,0,1]
	v_addc_co_u32_e32 v3, vcc, 0, v5, vcc
	s_andn2_b64 vcc, exec, s[2:3]
	s_mov_b64 s[2:3], -1
	global_store_dwordx4 v[2:3], v[6:9], off
	s_cbranch_vccnz .LBB0_1622
	s_andn2_b64 vcc, exec, s[6:7]
	s_cbranch_vccnz .LBB0_1621
	s_barrier
	s_branch .LBB0_1621
